# baseline (speedup 1.0000x reference)
_Z16bilateral_kernelPKfS0_Pf:
	s_load_dwordx2 s[4:5], s[0:1], 0x0
	s_load_dwordx2 s[8:9], s[0:1], 0x10
	s_lshr_b32 s19, s2, 8
	s_and_b32 s0, s2, 7
	s_mulk_i32 s0, 0x60
	s_lshr_b32 s1, s2, 3
	s_add_i32 s1, s0, s1
	s_lshr_b32 s0, s1, 6
	s_lshl_b32 s11, s1, 6
	s_nop 0
	s_and_b32 s11, s11, 0x1c0
	s_lshl_b32 s1, s1, 3
	s_nop 0
	s_and_b32 s10, s1, 0x1c0
	s_mov_b32 s1, 0
	s_lshl_b64 s[2:3], s[0:1], 20
	s_mov_b32 s20, 0xc05dfbe6
	s_mov_b32 s21, 0xc05dfbe6
	s_mov_b32 s22, 0xc0a8390e
	s_mov_b32 s23, 0xc0a8390e
	s_mov_b32 s24, 0xc08211a7
	s_mov_b32 s25, 0xc08211a7
	s_mov_b32 s26, 0xc0bb4cc1
	s_mov_b32 s27, 0xc0bb4cc1
	s_mov_b32 s28, 0xc0f487dc
	s_mov_b32 s29, 0xc0f487dc
	s_mov_b32 s30, 0x3e0bd796
	s_mov_b32 s31, 0x3e0bd796
	s_mov_b32 s32, 0x3f45a90c
	s_mov_b32 s33, 0x3f45a90c
	s_mov_b32 s34, 0x3fa5c782
	s_mov_b32 s35, 0x3fa5c782
	v_and_b32_e32 v134, 15, v0
	v_lshrrev_b32_e32 v131, 2, v0
	v_lshl_or_b32 v129, v134, 2, s11
	v_and_or_b32 v133, v131, 60, s10
	v_min_u32_e32 v132, 0x1fa, v129
	v_sub_u32_e64 v131, v129, 2 clamp
	v_add_u32_e64 v132, 4, v132
	v_cmp_eq_u32_e64 s[16:17], 0, v134
	v_cmp_eq_u32_e32 vcc, 15, v134
	s_nop 1
	v_cndmask_b32_e64 v131, v132, v131, s[16:17]
	s_or_b64 vcc, s[16:17], vcc
	v_lshlrev_b32_e32 v131, 2, v131
	v_mov_b32_e32 v132, 0x7ff00000
	s_nop 0
	v_cndmask_b32_e32 v128, v132, v131, vcc
	s_movk_i32 s18, 0x1fc
	v_cmp_eq_u32_e32 vcc, 0, v129
	v_cmp_eq_u32_e64 s[16:17], s18, v129
	v_lshlrev_b32_e32 v129, 2, v129
	s_waitcnt lgkmcnt(0)
	s_add_u32 s4, s4, s2
	s_addc_u32 s5, s5, s3
	s_and_b32 s5, s5, 0xffff
	s_mov_b32 s6, 0x100000
	s_mov_b32 s7, 0x20000
	s_add_u32 s12, s8, s2
	s_addc_u32 s13, s9, s3
	s_and_b32 s13, s13, 0xffff
	s_mov_b32 s14, 0x100000
	s_mov_b32 s15, 0x20000
	v_sub_u32_e64 v131, v133, 2 clamp
	v_lshlrev_b32_e32 v131, 11, v131
	v_add_u32_e32 v132, v131, v128
	v_add_u32_e64 v131, v131, v129
	buffer_load_dwordx2 v[0:1], v132, s[4:7], 0 offen nt
	buffer_load_dwordx2 v[6:7], v132, s[4:7], 0 offen nt
	buffer_load_dwordx4 v[2:5], v131, s[4:7], 0 offen nt
	v_sub_u32_e64 v131, v133, 1 clamp
	v_lshlrev_b32_e32 v131, 11, v131
	v_add_u32_e32 v132, v131, v128
	v_add_u32_e64 v131, v131, v129
	buffer_load_dwordx2 v[8:9], v132, s[4:7], 0 offen nt
	buffer_load_dwordx2 v[14:15], v132, s[4:7], 0 offen nt
	buffer_load_dwordx4 v[10:13], v131, s[4:7], 0 offen nt
	v_lshlrev_b32_e32 v131, 11, v133
	v_add_u32_e32 v132, v131, v128
	v_add_u32_e64 v130, v131, v129
	v_add_u32_e32 v135, 0x1000, v130
	buffer_load_dwordx2 v[16:17], v132, s[4:7], 0 offen nt
	buffer_load_dwordx2 v[22:23], v132, s[4:7], 0 offen nt
	buffer_load_dwordx4 v[18:21], v130, s[4:7], 0 offen nt
	v_lshlrev_b32_e64 v131, 11, v133
	v_add_u32_e32 v131, 0x800, v131
	v_add_u32_e32 v132, v131, v128
	v_add_u32_e32 v131, v131, v129
	buffer_load_dwordx2 v[24:25], v132, s[4:7], 0 offen nt
	buffer_load_dwordx2 v[30:31], v132, s[4:7], 0 offen nt
	buffer_load_dwordx4 v[26:29], v131, s[4:7], 0 offen nt
	v_lshlrev_b32_e64 v131, 11, v133
	v_add_u32_e32 v131, 0x1000, v131
	v_add_u32_e32 v132, v131, v128
	v_add_u32_e32 v131, v131, v129
	buffer_load_dwordx2 v[32:33], v132, s[4:7], 0 offen nt
	buffer_load_dwordx2 v[38:39], v132, s[4:7], 0 offen nt
	buffer_load_dwordx4 v[34:37], v131, s[4:7], 0 offen nt
	v_lshlrev_b32_e64 v131, 11, v133
	v_add_u32_e32 v131, 0x1800, v131
	v_add_u32_e32 v132, v131, v128
	v_add_u32_e32 v131, v131, v129
	buffer_load_dwordx2 v[40:41], v132, s[4:7], 0 offen nt
	buffer_load_dwordx2 v[46:47], v132, s[4:7], 0 offen nt
	buffer_load_dwordx4 v[42:45], v131, s[4:7], 0 offen nt
	v_min_u32_e32 v131, 0x1fb, v133
	v_lshlrev_b32_e64 v131, 11, v131
	v_add_u32_e32 v131, 0x2000, v131
	v_add_u32_e32 v132, v131, v128
	v_add_u32_e32 v131, v131, v129
	buffer_load_dwordx2 v[48:49], v132, s[4:7], 0 offen nt
	buffer_load_dwordx2 v[54:55], v132, s[4:7], 0 offen nt
	buffer_load_dwordx4 v[50:53], v131, s[4:7], 0 offen nt
	v_min_u32_e32 v131, 0x1fa, v133
	v_lshlrev_b32_e64 v131, 11, v131
	v_add_u32_e32 v131, 0x2800, v131
	v_add_u32_e32 v132, v131, v128
	v_add_u32_e32 v131, v131, v129
	buffer_load_dwordx2 v[56:57], v132, s[4:7], 0 offen nt
	buffer_load_dwordx2 v[62:63], v132, s[4:7], 0 offen nt
	buffer_load_dwordx4 v[58:61], v131, s[4:7], 0 offen nt
	s_cmp_eq_u32 s19, 0
	s_cbranch_scc1 .Lmyp0
	s_cmp_eq_u32 s19, 1
	s_cbranch_scc1 .Lmyp1
	s_setprio 0
	s_branch .Lmypd

.Lmypd:
	s_waitcnt vmcnt(21)
	v_mov_b32_dpp v0, v4 row_shr:1 row_mask:0xf bank_mask:0xf
	v_mov_b32_dpp v1, v5 row_shr:1 row_mask:0xf bank_mask:0xf
	v_mov_b32_dpp v6, v2 row_shl:1 row_mask:0xf bank_mask:0xf
	v_mov_b32_dpp v7, v3 row_shl:1 row_mask:0xf bank_mask:0xf
	v_pk_mul_f32 v[2:3], v[2:3], s[32:33]
	v_pk_mul_f32 v[4:5], v[4:5], s[32:33]
	v_cndmask_b32_e64 v1, v1, v0, vcc
	v_cndmask_b32_e64 v6, v6, v7, s[16:17]
	v_pk_mul_f32 v[0:1], v[0:1], s[32:33]
	v_pk_mul_f32 v[6:7], v[6:7], s[32:33]
	s_waitcnt vmcnt(18)
	s_nop 0
	v_mov_b32_dpp v8, v12 row_shr:1 row_mask:0xf bank_mask:0xf
	v_mov_b32_dpp v9, v13 row_shr:1 row_mask:0xf bank_mask:0xf
	v_mov_b32_dpp v14, v10 row_shl:1 row_mask:0xf bank_mask:0xf
	v_mov_b32_dpp v15, v11 row_shl:1 row_mask:0xf bank_mask:0xf
	v_pk_mul_f32 v[10:11], v[10:11], s[32:33]
	v_pk_mul_f32 v[12:13], v[12:13], s[32:33]
	v_cndmask_b32_e64 v9, v9, v8, vcc
	v_cndmask_b32_e64 v14, v14, v15, s[16:17]
	v_pk_mul_f32 v[8:9], v[8:9], s[32:33]
	v_pk_mul_f32 v[14:15], v[14:15], s[32:33]
	s_waitcnt vmcnt(15)
	s_nop 0
	v_mov_b32_dpp v16, v20 row_shr:1 row_mask:0xf bank_mask:0xf
	v_mov_b32_dpp v17, v21 row_shr:1 row_mask:0xf bank_mask:0xf
	v_mov_b32_dpp v22, v18 row_shl:1 row_mask:0xf bank_mask:0xf
	v_mov_b32_dpp v23, v19 row_shl:1 row_mask:0xf bank_mask:0xf
	v_pk_mul_f32 v[18:19], v[18:19], s[32:33]
	v_pk_mul_f32 v[20:21], v[20:21], s[32:33]
	v_cndmask_b32_e64 v17, v17, v16, vcc
	v_cndmask_b32_e64 v22, v22, v23, s[16:17]
	v_pk_mul_f32 v[68:69], v[18:19], s[30:31]
	v_pk_mul_f32 v[70:71], v[20:21], s[30:31]
	v_pk_mul_f32 v[16:17], v[16:17], s[32:33]
	v_pk_mul_f32 v[22:23], v[22:23], s[32:33]
	v_pk_add_f32 v[96:97], v[18:19], v[0:1] neg_lo:[0,1] neg_hi:[0,1]
	v_pk_add_f32 v[98:99], v[18:19], v[2:3] neg_lo:[0,1] neg_hi:[0,1]
	v_pk_add_f32 v[100:101], v[20:21], v[2:3] neg_lo:[0,1] neg_hi:[0,1]
	v_pk_add_f32 v[102:103], v[18:19], v[4:5] neg_lo:[0,1] neg_hi:[0,1]
	v_pk_add_f32 v[104:105], v[20:21], v[4:5] neg_lo:[0,1] neg_hi:[0,1]
	v_pk_add_f32 v[106:107], v[20:21], v[6:7] neg_lo:[0,1] neg_hi:[0,1]
	v_pk_add_f32 v[108:109], v[18:19], v[2:3] op_sel:[1,0] op_sel_hi:[0,1] neg_lo:[0,1] neg_hi:[0,1]
	v_pk_add_f32 v[110:111], v[20:21], v[4:5] op_sel:[1,0] op_sel_hi:[0,1] neg_lo:[0,1] neg_hi:[0,1]
	v_pk_fma_f32 v[96:97], v[96:97], v[96:97], s[28:29] neg_lo:[1,0,0] neg_hi:[1,0,0]
	v_pk_fma_f32 v[98:99], v[98:99], v[98:99], s[22:23] neg_lo:[1,0,0] neg_hi:[1,0,0]
	v_pk_fma_f32 v[100:101], v[100:101], v[100:101], s[28:29] neg_lo:[1,0,0] neg_hi:[1,0,0]
	v_pk_fma_f32 v[102:103], v[102:103], v[102:103], s[28:29] neg_lo:[1,0,0] neg_hi:[1,0,0]
	v_pk_fma_f32 v[104:105], v[104:105], v[104:105], s[22:23] neg_lo:[1,0,0] neg_hi:[1,0,0]
	v_pk_fma_f32 v[106:107], v[106:107], v[106:107], s[28:29] neg_lo:[1,0,0] neg_hi:[1,0,0]
	v_pk_fma_f32 v[108:109], v[108:109], v[108:109], s[26:27] neg_lo:[1,0,0] neg_hi:[1,0,0]
	v_pk_fma_f32 v[110:111], v[110:111], v[110:111], s[26:27] neg_lo:[1,0,0] neg_hi:[1,0,0]
	v_exp_f32_e32 v96, v96
	v_exp_f32_e32 v97, v97
	v_exp_f32_e32 v98, v98
	v_exp_f32_e32 v99, v99
	v_exp_f32_e32 v100, v100
	v_exp_f32_e32 v101, v101
	v_exp_f32_e32 v102, v102
	v_exp_f32_e32 v103, v103
	v_exp_f32_e32 v104, v104
	v_exp_f32_e32 v105, v105
	v_exp_f32_e32 v106, v106
	v_exp_f32_e32 v107, v107
	v_exp_f32_e32 v108, v108
	v_exp_f32_e32 v109, v109
	v_exp_f32_e32 v110, v110
	v_exp_f32_e32 v111, v111
	v_pk_add_f32 v[112:113], v[18:19], v[8:9] neg_lo:[0,1] neg_hi:[0,1]
	v_pk_add_f32 v[114:115], v[18:19], v[10:11] neg_lo:[0,1] neg_hi:[0,1]
	v_pk_add_f32 v[116:117], v[20:21], v[10:11] neg_lo:[0,1] neg_hi:[0,1]
	v_pk_add_f32 v[118:119], v[18:19], v[12:13] neg_lo:[0,1] neg_hi:[0,1]
	v_pk_add_f32 v[120:121], v[20:21], v[12:13] neg_lo:[0,1] neg_hi:[0,1]
	v_pk_add_f32 v[122:123], v[20:21], v[14:15] neg_lo:[0,1] neg_hi:[0,1]
	v_pk_add_f32 v[124:125], v[18:19], v[10:11] op_sel:[1,0] op_sel_hi:[0,1] neg_lo:[0,1] neg_hi:[0,1]
	v_pk_add_f32 v[126:127], v[20:21], v[12:13] op_sel:[1,0] op_sel_hi:[0,1] neg_lo:[0,1] neg_hi:[0,1]
	v_pk_fma_f32 v[112:113], v[112:113], v[112:113], s[26:27] neg_lo:[1,0,0] neg_hi:[1,0,0]
	v_pk_fma_f32 v[114:115], v[114:115], v[114:115], s[20:21] neg_lo:[1,0,0] neg_hi:[1,0,0]
	v_pk_fma_f32 v[116:117], v[116:117], v[116:117], s[26:27] neg_lo:[1,0,0] neg_hi:[1,0,0]
	v_pk_fma_f32 v[118:119], v[118:119], v[118:119], s[26:27] neg_lo:[1,0,0] neg_hi:[1,0,0]
	v_pk_fma_f32 v[120:121], v[120:121], v[120:121], s[20:21] neg_lo:[1,0,0] neg_hi:[1,0,0]
	v_pk_fma_f32 v[122:123], v[122:123], v[122:123], s[26:27] neg_lo:[1,0,0] neg_hi:[1,0,0]
	v_pk_fma_f32 v[124:125], v[124:125], v[124:125], s[24:25] neg_lo:[1,0,0] neg_hi:[1,0,0]
	v_pk_fma_f32 v[126:127], v[126:127], v[126:127], s[24:25] neg_lo:[1,0,0] neg_hi:[1,0,0]
	v_exp_f32_e32 v112, v112
	v_exp_f32_e32 v113, v113
	v_exp_f32_e32 v114, v114
	v_exp_f32_e32 v115, v115
	v_exp_f32_e32 v116, v116
	v_exp_f32_e32 v117, v117
	v_exp_f32_e32 v118, v118
	v_exp_f32_e32 v119, v119
	v_exp_f32_e32 v120, v120
	v_exp_f32_e32 v121, v121
	v_exp_f32_e32 v122, v122
	v_exp_f32_e32 v123, v123
	v_exp_f32_e32 v124, v124
	v_exp_f32_e32 v125, v125
	v_exp_f32_e32 v126, v126
	v_exp_f32_e32 v127, v127
	v_pk_add_f32 v[64:65], s[30:31], v[96:97]
	v_pk_fma_f32 v[68:69], v[96:97], v[0:1], v[68:69]
	v_pk_add_f32 v[66:67], s[30:31], v[100:101]
	v_pk_add_f32 v[64:65], v[64:65], v[98:99]
	v_pk_fma_f32 v[68:69], v[98:99], v[2:3], v[68:69]
	v_pk_fma_f32 v[70:71], v[100:101], v[2:3], v[70:71]
	v_pk_add_f32 v[64:65], v[64:65], v[102:103]
	v_pk_fma_f32 v[68:69], v[102:103], v[4:5], v[68:69]
	v_pk_add_f32 v[66:67], v[66:67], v[104:105]
	v_pk_fma_f32 v[70:71], v[104:105], v[4:5], v[70:71]
	v_pk_add_f32 v[64:65], v[64:65], v[108:109] op_sel:[0,1] op_sel_hi:[1,0]
	v_pk_add_f32 v[66:67], v[66:67], v[106:107]
	v_pk_fma_f32 v[70:71], v[106:107], v[6:7], v[70:71]
	v_pk_fma_f32 v[68:69], v[108:109], v[2:3], v[68:69] op_sel:[1,1,0] op_sel_hi:[0,0,1]
	v_pk_add_f32 v[66:67], v[66:67], v[110:111] op_sel:[0,1] op_sel_hi:[1,0]
	v_pk_fma_f32 v[70:71], v[110:111], v[4:5], v[70:71] op_sel:[1,1,0] op_sel_hi:[0,0,1]
	v_pk_add_f32 v[96:97], v[18:19], v[16:17] neg_lo:[0,1] neg_hi:[0,1]
	v_pk_add_f32 v[98:99], v[20:21], v[18:19] neg_lo:[0,1] neg_hi:[0,1]
	v_pk_add_f32 v[100:101], v[22:23], v[20:21] neg_lo:[0,1] neg_hi:[0,1]
	v_pk_fma_f32 v[96:97], v[96:97], v[96:97], s[22:23] neg_lo:[1,0,0] neg_hi:[1,0,0]
	v_pk_fma_f32 v[98:99], v[98:99], v[98:99], s[22:23] neg_lo:[1,0,0] neg_hi:[1,0,0]
	v_pk_fma_f32 v[100:101], v[100:101], v[100:101], s[22:23] neg_lo:[1,0,0] neg_hi:[1,0,0]
	v_exp_f32_e32 v96, v96
	v_exp_f32_e32 v97, v97
	v_exp_f32_e32 v98, v98
	v_exp_f32_e32 v99, v99
	v_exp_f32_e32 v100, v100
	v_exp_f32_e32 v101, v101
	v_pk_add_f32 v[64:65], v[64:65], v[112:113]
	v_pk_fma_f32 v[68:69], v[112:113], v[8:9], v[68:69]
	v_pk_add_f32 v[66:67], v[66:67], v[116:117]
	v_pk_add_f32 v[64:65], v[64:65], v[114:115]
	v_pk_fma_f32 v[68:69], v[114:115], v[10:11], v[68:69]
	v_pk_fma_f32 v[70:71], v[116:117], v[10:11], v[70:71]
	v_pk_add_f32 v[64:65], v[64:65], v[118:119]
	v_pk_fma_f32 v[68:69], v[118:119], v[12:13], v[68:69]
	v_pk_add_f32 v[66:67], v[66:67], v[120:121]
	v_pk_fma_f32 v[70:71], v[120:121], v[12:13], v[70:71]
	v_pk_add_f32 v[64:65], v[64:65], v[124:125] op_sel:[0,1] op_sel_hi:[1,0]
	v_pk_add_f32 v[66:67], v[66:67], v[122:123]
	v_pk_fma_f32 v[70:71], v[122:123], v[14:15], v[70:71]
	v_pk_fma_f32 v[68:69], v[124:125], v[10:11], v[68:69] op_sel:[1,1,0] op_sel_hi:[0,0,1]
	v_pk_add_f32 v[66:67], v[66:67], v[126:127] op_sel:[0,1] op_sel_hi:[1,0]
	v_pk_fma_f32 v[70:71], v[126:127], v[12:13], v[70:71] op_sel:[1,1,0] op_sel_hi:[0,0,1]
	v_sub_f32_e32 v116, v18, v1
	v_sub_f32_e32 v118, v20, v3
	v_sub_f32_e32 v120, v19, v4
	v_sub_f32_e32 v122, v21, v6
	v_sub_f32_e32 v124, v18, v9
	v_sub_f32_e32 v126, v20, v11
	v_sub_f32_e32 v113, v19, v12
	v_sub_f32_e32 v115, v21, v14
	v_sub_f32_e32 v117, v18, v17
	v_sub_f32_e32 v112, v19, v18
	v_sub_f32_e32 v119, v20, v19
	v_sub_f32_e32 v114, v21, v20
	v_sub_f32_e64 v121, v22, v21
	v_fma_f32 v116, -v116, v116, s26
	v_fma_f32 v118, -v118, v118, s26
	v_fma_f32 v120, -v120, v120, s26
	v_fma_f32 v122, -v122, v122, s26
	v_fma_f32 v124, -v124, v124, s24
	v_fma_f32 v126, -v126, v126, s24
	v_fma_f32 v113, -v113, v113, s24
	v_fma_f32 v115, -v115, v115, s24
	v_fma_f32 v117, -v117, v117, s20
	v_fma_f32 v112, -v112, v112, s20
	v_fma_f32 v119, -v119, v119, s20
	v_fma_f32 v114, -v114, v114, s20
	v_fma_f32 v121, -v121, v121, s20
	v_exp_f32_e32 v116, v116
	v_exp_f32_e32 v118, v118
	v_exp_f32_e32 v120, v120
	v_exp_f32_e32 v122, v122
	v_exp_f32_e32 v124, v124
	v_exp_f32_e32 v126, v126
	v_exp_f32_e32 v113, v113
	v_exp_f32_e32 v115, v115
	v_exp_f32_e32 v117, v117
	v_exp_f32_e32 v112, v112
	v_exp_f32_e32 v119, v119
	v_exp_f32_e32 v114, v114
	v_exp_f32_e64 v121, v121
	v_pk_add_f32 v[64:65], v[64:65], v[96:97]
	v_pk_fma_f32 v[68:69], v[96:97], v[16:17], v[68:69]
	v_pk_add_f32 v[66:67], v[66:67], v[98:99]
	v_pk_add_f32 v[64:65], v[64:65], v[98:99]
	v_pk_fma_f32 v[68:69], v[98:99], v[20:21], v[68:69]
	v_pk_fma_f32 v[70:71], v[98:99], v[18:19], v[70:71]
	v_pk_add_f32 v[66:67], v[66:67], v[100:101]
	v_pk_fma_f32 v[70:71], v[100:101], v[22:23], v[70:71]
	v_add_f32_e32 v64, v64, v116
	v_fmac_f32_e32 v68, v116, v1
	v_add_f32_e32 v66, v66, v118
	v_fmac_f32_e32 v70, v118, v3
	v_add_f32_e32 v65, v65, v120
	v_fmac_f32_e32 v69, v120, v4
	v_add_f32_e32 v67, v67, v122
	v_fmac_f32_e32 v71, v122, v6
	v_add_f32_e32 v64, v64, v124
	v_fmac_f32_e32 v68, v124, v9
	v_add_f32_e32 v66, v66, v126
	v_fmac_f32_e32 v70, v126, v11
	v_add_f32_e32 v65, v65, v113
	v_fmac_f32_e32 v69, v113, v12
	v_add_f32_e32 v67, v67, v115
	v_fmac_f32_e32 v71, v115, v14
	v_add_f32_e32 v64, v64, v117
	v_fmac_f32_e32 v68, v117, v17
	v_add_f32_e32 v65, v65, v119
	v_fmac_f32_e32 v69, v119, v20
	v_add_f32_e32 v66, v66, v119
	v_fmac_f32_e32 v70, v119, v19
	v_add_f32_e32 v67, v67, v121
	v_fmac_f32_e32 v71, v121, v22
	v_pk_add_f32 v[64:65], v[64:65], v[112:113] op_sel_hi:[1,0]
	v_pk_fma_f32 v[68:69], v[112:113], v[18:19], v[68:69] op_sel:[0,1,0] op_sel_hi:[0,0,1]
	v_pk_add_f32 v[66:67], v[66:67], v[114:115] op_sel_hi:[1,0]
	v_pk_fma_f32 v[70:71], v[114:115], v[20:21], v[70:71] op_sel:[0,1,0] op_sel_hi:[0,0,1]
	s_waitcnt vmcnt(12)
	s_nop 0
	v_mov_b32_dpp v24, v28 row_shr:1 row_mask:0xf bank_mask:0xf
	v_mov_b32_dpp v25, v29 row_shr:1 row_mask:0xf bank_mask:0xf
	v_mov_b32_dpp v30, v26 row_shl:1 row_mask:0xf bank_mask:0xf
	v_mov_b32_dpp v31, v27 row_shl:1 row_mask:0xf bank_mask:0xf
	v_pk_mul_f32 v[26:27], v[26:27], s[32:33]
	v_pk_mul_f32 v[28:29], v[28:29], s[32:33]
	v_cndmask_b32_e64 v25, v25, v24, vcc
	v_cndmask_b32_e64 v30, v30, v31, s[16:17]
	v_pk_mul_f32 v[76:77], v[26:27], s[30:31]
	v_pk_mul_f32 v[78:79], v[28:29], s[30:31]
	v_pk_mul_f32 v[24:25], v[24:25], s[32:33]
	v_pk_mul_f32 v[30:31], v[30:31], s[32:33]
	v_pk_add_f32 v[96:97], v[26:27], v[8:9] neg_lo:[0,1] neg_hi:[0,1]
	v_pk_add_f32 v[98:99], v[26:27], v[10:11] neg_lo:[0,1] neg_hi:[0,1]
	v_pk_add_f32 v[100:101], v[28:29], v[10:11] neg_lo:[0,1] neg_hi:[0,1]
	v_pk_add_f32 v[102:103], v[26:27], v[12:13] neg_lo:[0,1] neg_hi:[0,1]
	v_pk_add_f32 v[104:105], v[28:29], v[12:13] neg_lo:[0,1] neg_hi:[0,1]
	v_pk_add_f32 v[106:107], v[28:29], v[14:15] neg_lo:[0,1] neg_hi:[0,1]
	v_pk_add_f32 v[108:109], v[26:27], v[10:11] op_sel:[1,0] op_sel_hi:[0,1] neg_lo:[0,1] neg_hi:[0,1]
	v_pk_add_f32 v[110:111], v[28:29], v[12:13] op_sel:[1,0] op_sel_hi:[0,1] neg_lo:[0,1] neg_hi:[0,1]
	v_pk_fma_f32 v[96:97], v[96:97], v[96:97], s[28:29] neg_lo:[1,0,0] neg_hi:[1,0,0]
	v_pk_fma_f32 v[98:99], v[98:99], v[98:99], s[22:23] neg_lo:[1,0,0] neg_hi:[1,0,0]
	v_pk_fma_f32 v[100:101], v[100:101], v[100:101], s[28:29] neg_lo:[1,0,0] neg_hi:[1,0,0]
	v_pk_fma_f32 v[102:103], v[102:103], v[102:103], s[28:29] neg_lo:[1,0,0] neg_hi:[1,0,0]
	v_pk_fma_f32 v[104:105], v[104:105], v[104:105], s[22:23] neg_lo:[1,0,0] neg_hi:[1,0,0]
	v_pk_fma_f32 v[106:107], v[106:107], v[106:107], s[28:29] neg_lo:[1,0,0] neg_hi:[1,0,0]
	v_pk_fma_f32 v[108:109], v[108:109], v[108:109], s[26:27] neg_lo:[1,0,0] neg_hi:[1,0,0]
	v_pk_fma_f32 v[110:111], v[110:111], v[110:111], s[26:27] neg_lo:[1,0,0] neg_hi:[1,0,0]
	v_exp_f32_e32 v96, v96
	v_exp_f32_e32 v97, v97
	v_exp_f32_e32 v98, v98
	v_exp_f32_e32 v99, v99
	v_exp_f32_e32 v100, v100
	v_exp_f32_e32 v101, v101
	v_exp_f32_e32 v102, v102
	v_exp_f32_e32 v103, v103
	v_exp_f32_e32 v104, v104
	v_exp_f32_e32 v105, v105
	v_exp_f32_e32 v106, v106
	v_exp_f32_e32 v107, v107
	v_exp_f32_e32 v108, v108
	v_exp_f32_e32 v109, v109
	v_exp_f32_e32 v110, v110
	v_exp_f32_e32 v111, v111
	v_pk_add_f32 v[112:113], v[26:27], v[16:17] neg_lo:[0,1] neg_hi:[0,1]
	v_pk_add_f32 v[114:115], v[24:25], v[18:19] neg_lo:[0,1] neg_hi:[0,1]
	v_pk_add_f32 v[116:117], v[26:27], v[18:19] neg_lo:[0,1] neg_hi:[0,1]
	v_pk_add_f32 v[118:119], v[28:29], v[18:19] neg_lo:[0,1] neg_hi:[0,1]
	v_pk_add_f32 v[120:121], v[26:27], v[20:21] neg_lo:[0,1] neg_hi:[0,1]
	v_pk_add_f32 v[122:123], v[28:29], v[20:21] neg_lo:[0,1] neg_hi:[0,1]
	v_pk_add_f32 v[124:125], v[30:31], v[20:21] neg_lo:[0,1] neg_hi:[0,1]
	v_pk_add_f32 v[126:127], v[28:29], v[22:23] neg_lo:[0,1] neg_hi:[0,1]
	v_pk_fma_f32 v[112:113], v[112:113], v[112:113], s[26:27] neg_lo:[1,0,0] neg_hi:[1,0,0]
	v_pk_fma_f32 v[114:115], v[114:115], v[114:115], s[26:27] neg_lo:[1,0,0] neg_hi:[1,0,0]
	v_pk_fma_f32 v[116:117], v[116:117], v[116:117], s[20:21] neg_lo:[1,0,0] neg_hi:[1,0,0]
	v_pk_fma_f32 v[118:119], v[118:119], v[118:119], s[26:27] neg_lo:[1,0,0] neg_hi:[1,0,0]
	v_pk_fma_f32 v[120:121], v[120:121], v[120:121], s[26:27] neg_lo:[1,0,0] neg_hi:[1,0,0]
	v_pk_fma_f32 v[122:123], v[122:123], v[122:123], s[20:21] neg_lo:[1,0,0] neg_hi:[1,0,0]
	v_pk_fma_f32 v[124:125], v[124:125], v[124:125], s[26:27] neg_lo:[1,0,0] neg_hi:[1,0,0]
	v_pk_fma_f32 v[126:127], v[126:127], v[126:127], s[26:27] neg_lo:[1,0,0] neg_hi:[1,0,0]
	v_exp_f32_e32 v112, v112
	v_exp_f32_e32 v113, v113
	v_exp_f32_e32 v114, v114
	v_exp_f32_e32 v115, v115
	v_exp_f32_e32 v116, v116
	v_exp_f32_e32 v117, v117
	v_exp_f32_e32 v118, v118
	v_exp_f32_e32 v119, v119
	v_exp_f32_e32 v120, v120
	v_exp_f32_e32 v121, v121
	v_exp_f32_e32 v122, v122
	v_exp_f32_e32 v123, v123
	v_exp_f32_e32 v124, v124
	v_exp_f32_e32 v125, v125
	v_exp_f32_e32 v126, v126
	v_exp_f32_e32 v127, v127
	v_pk_add_f32 v[72:73], s[30:31], v[96:97]
	v_pk_fma_f32 v[76:77], v[96:97], v[8:9], v[76:77]
	v_pk_add_f32 v[74:75], s[30:31], v[100:101]
	v_pk_add_f32 v[72:73], v[72:73], v[98:99]
	v_pk_fma_f32 v[76:77], v[98:99], v[10:11], v[76:77]
	v_pk_fma_f32 v[78:79], v[100:101], v[10:11], v[78:79]
	v_pk_add_f32 v[72:73], v[72:73], v[102:103]
	v_pk_fma_f32 v[76:77], v[102:103], v[12:13], v[76:77]
	v_pk_add_f32 v[74:75], v[74:75], v[104:105]
	v_pk_fma_f32 v[78:79], v[104:105], v[12:13], v[78:79]
	v_pk_add_f32 v[72:73], v[72:73], v[108:109] op_sel:[0,1] op_sel_hi:[1,0]
	v_pk_add_f32 v[74:75], v[74:75], v[106:107]
	v_pk_fma_f32 v[78:79], v[106:107], v[14:15], v[78:79]
	v_pk_fma_f32 v[76:77], v[108:109], v[10:11], v[76:77] op_sel:[1,1,0] op_sel_hi:[0,0,1]
	v_pk_add_f32 v[74:75], v[74:75], v[110:111] op_sel:[0,1] op_sel_hi:[1,0]
	v_pk_fma_f32 v[78:79], v[110:111], v[12:13], v[78:79] op_sel:[1,1,0] op_sel_hi:[0,0,1]
	v_pk_add_f32 v[96:97], v[26:27], v[18:19] op_sel:[1,0] op_sel_hi:[0,1] neg_lo:[0,1] neg_hi:[0,1]
	v_pk_add_f32 v[98:99], v[28:29], v[20:21] op_sel:[1,0] op_sel_hi:[0,1] neg_lo:[0,1] neg_hi:[0,1]
	v_pk_add_f32 v[100:101], v[26:27], v[24:25] neg_lo:[0,1] neg_hi:[0,1]
	v_pk_add_f32 v[102:103], v[28:29], v[26:27] neg_lo:[0,1] neg_hi:[0,1]
	v_pk_add_f32 v[104:105], v[30:31], v[28:29] neg_lo:[0,1] neg_hi:[0,1]
	v_pk_fma_f32 v[96:97], v[96:97], v[96:97], s[24:25] neg_lo:[1,0,0] neg_hi:[1,0,0]
	v_pk_fma_f32 v[98:99], v[98:99], v[98:99], s[24:25] neg_lo:[1,0,0] neg_hi:[1,0,0]
	v_pk_fma_f32 v[100:101], v[100:101], v[100:101], s[22:23] neg_lo:[1,0,0] neg_hi:[1,0,0]
	v_pk_fma_f32 v[102:103], v[102:103], v[102:103], s[22:23] neg_lo:[1,0,0] neg_hi:[1,0,0]
	v_pk_fma_f32 v[104:105], v[104:105], v[104:105], s[22:23] neg_lo:[1,0,0] neg_hi:[1,0,0]
	v_exp_f32_e32 v96, v96
	v_exp_f32_e32 v97, v97
	v_exp_f32_e32 v98, v98
	v_exp_f32_e32 v99, v99
	v_exp_f32_e32 v100, v100
	v_exp_f32_e32 v101, v101
	v_exp_f32_e32 v102, v102
	v_exp_f32_e32 v103, v103
	v_exp_f32_e32 v104, v104
	v_exp_f32_e32 v105, v105
	v_pk_add_f32 v[72:73], v[72:73], v[112:113]
	v_pk_fma_f32 v[76:77], v[112:113], v[16:17], v[76:77]
	v_pk_add_f32 v[64:65], v[64:65], v[114:115]
	v_pk_fma_f32 v[68:69], v[114:115], v[24:25], v[68:69]
	v_pk_add_f32 v[72:73], v[72:73], v[116:117]
	v_pk_add_f32 v[64:65], v[64:65], v[116:117]
	v_pk_fma_f32 v[68:69], v[116:117], v[26:27], v[68:69]
	v_pk_fma_f32 v[76:77], v[116:117], v[18:19], v[76:77]
	v_pk_add_f32 v[64:65], v[64:65], v[118:119]
	v_pk_fma_f32 v[68:69], v[118:119], v[28:29], v[68:69]
	v_pk_add_f32 v[74:75], v[74:75], v[118:119]
	v_pk_fma_f32 v[78:79], v[118:119], v[18:19], v[78:79]
	v_pk_add_f32 v[66:67], v[66:67], v[120:121]
	v_pk_fma_f32 v[70:71], v[120:121], v[26:27], v[70:71]
	v_pk_add_f32 v[72:73], v[72:73], v[120:121]
	v_pk_fma_f32 v[76:77], v[120:121], v[20:21], v[76:77]
	v_pk_add_f32 v[66:67], v[66:67], v[122:123]
	v_pk_fma_f32 v[70:71], v[122:123], v[28:29], v[70:71]
	v_pk_add_f32 v[74:75], v[74:75], v[122:123]
	v_pk_fma_f32 v[78:79], v[122:123], v[20:21], v[78:79]
	v_pk_add_f32 v[66:67], v[66:67], v[124:125]
	v_pk_fma_f32 v[70:71], v[124:125], v[30:31], v[70:71]
	v_pk_add_f32 v[74:75], v[74:75], v[126:127]
	v_pk_fma_f32 v[78:79], v[126:127], v[22:23], v[78:79]
	v_sub_f32_e32 v116, v26, v9
	v_sub_f32_e32 v118, v28, v11
	v_sub_f32_e32 v120, v27, v12
	v_sub_f32_e32 v122, v29, v14
	v_sub_f32_e32 v124, v26, v17
	v_sub_f32_e32 v126, v25, v18
	v_sub_f32_e32 v113, v28, v19
	v_sub_f32_e32 v115, v27, v20
	v_sub_f32_e32 v117, v30, v21
	v_sub_f32_e32 v119, v29, v22
	v_sub_f32_e32 v121, v26, v25
	v_sub_f32_e32 v112, v27, v26
	v_sub_f32_e32 v123, v28, v27
	v_sub_f32_e32 v114, v29, v28
	v_sub_f32_e64 v125, v30, v29
	v_fma_f32 v116, -v116, v116, s26
	v_fma_f32 v118, -v118, v118, s26
	v_fma_f32 v120, -v120, v120, s26
	v_fma_f32 v122, -v122, v122, s26
	v_fma_f32 v124, -v124, v124, s24
	v_fma_f32 v126, -v126, v126, s24
	v_fma_f32 v113, -v113, v113, s24
	v_fma_f32 v115, -v115, v115, s24
	v_fma_f32 v117, -v117, v117, s24
	v_fma_f32 v119, -v119, v119, s24
	v_fma_f32 v121, -v121, v121, s20
	v_fma_f32 v112, -v112, v112, s20
	v_fma_f32 v123, -v123, v123, s20
	v_fma_f32 v114, -v114, v114, s20
	v_fma_f32 v125, -v125, v125, s20
	v_exp_f32_e32 v116, v116
	v_exp_f32_e32 v118, v118
	v_exp_f32_e32 v120, v120
	v_exp_f32_e32 v122, v122
	v_exp_f32_e32 v124, v124
	v_exp_f32_e32 v126, v126
	v_exp_f32_e32 v113, v113
	v_exp_f32_e32 v115, v115
	v_exp_f32_e32 v117, v117
	v_exp_f32_e32 v119, v119
	v_exp_f32_e32 v121, v121
	v_exp_f32_e32 v112, v112
	v_exp_f32_e32 v123, v123
	v_exp_f32_e32 v114, v114
	v_exp_f32_e64 v125, v125
	v_pk_add_f32 v[64:65], v[64:65], v[96:97]
	v_pk_fma_f32 v[68:69], v[96:97], v[26:27], v[68:69] op_sel:[0,1,0] op_sel_hi:[1,0,1]
	v_pk_add_f32 v[72:73], v[72:73], v[96:97] op_sel:[0,1] op_sel_hi:[1,0]
	v_pk_fma_f32 v[76:77], v[96:97], v[18:19], v[76:77] op_sel:[1,1,0] op_sel_hi:[0,0,1]
	v_pk_add_f32 v[66:67], v[66:67], v[98:99]
	v_pk_fma_f32 v[70:71], v[98:99], v[28:29], v[70:71] op_sel:[0,1,0] op_sel_hi:[1,0,1]
	v_pk_add_f32 v[74:75], v[74:75], v[98:99] op_sel:[0,1] op_sel_hi:[1,0]
	v_pk_fma_f32 v[78:79], v[98:99], v[20:21], v[78:79] op_sel:[1,1,0] op_sel_hi:[0,0,1]
	v_pk_add_f32 v[72:73], v[72:73], v[100:101]
	v_pk_fma_f32 v[76:77], v[100:101], v[24:25], v[76:77]
	v_pk_add_f32 v[74:75], v[74:75], v[102:103]
	v_pk_add_f32 v[72:73], v[72:73], v[102:103]
	v_pk_fma_f32 v[76:77], v[102:103], v[28:29], v[76:77]
	v_pk_fma_f32 v[78:79], v[102:103], v[26:27], v[78:79]
	v_pk_add_f32 v[74:75], v[74:75], v[104:105]
	v_pk_fma_f32 v[78:79], v[104:105], v[30:31], v[78:79]
	v_add_f32_e32 v72, v72, v116
	v_fmac_f32_e32 v76, v116, v9
	v_add_f32_e32 v74, v74, v118
	v_fmac_f32_e32 v78, v118, v11
	v_add_f32_e32 v73, v73, v120
	v_fmac_f32_e32 v77, v120, v12
	v_add_f32_e32 v75, v75, v122
	v_fmac_f32_e32 v79, v122, v14
	v_add_f32_e32 v72, v72, v124
	v_fmac_f32_e32 v76, v124, v17
	v_add_f32_e32 v64, v64, v126
	v_fmac_f32_e32 v68, v126, v25
	v_add_f32_e32 v65, v65, v113
	v_fmac_f32_e32 v69, v113, v28
	v_add_f32_e32 v74, v74, v113
	v_fmac_f32_e32 v78, v113, v19
	v_add_f32_e32 v66, v66, v115
	v_fmac_f32_e32 v70, v115, v27
	v_add_f32_e32 v73, v73, v115
	v_fmac_f32_e32 v77, v115, v20
	v_add_f32_e32 v67, v67, v117
	v_fmac_f32_e32 v71, v117, v30
	v_add_f32_e32 v75, v75, v119
	v_fmac_f32_e32 v79, v119, v22
	v_add_f32_e32 v72, v72, v121
	v_fmac_f32_e32 v76, v121, v25
	v_add_f32_e32 v73, v73, v123
	v_fmac_f32_e32 v77, v123, v28
	v_add_f32_e32 v74, v74, v123
	v_fmac_f32_e32 v78, v123, v27
	v_add_f32_e32 v75, v75, v125
	v_fmac_f32_e32 v79, v125, v30
	v_pk_add_f32 v[72:73], v[72:73], v[112:113] op_sel_hi:[1,0]
	v_pk_fma_f32 v[76:77], v[112:113], v[26:27], v[76:77] op_sel:[0,1,0] op_sel_hi:[0,0,1]
	v_pk_add_f32 v[74:75], v[74:75], v[114:115] op_sel_hi:[1,0]
	v_pk_fma_f32 v[78:79], v[114:115], v[28:29], v[78:79] op_sel:[0,1,0] op_sel_hi:[0,0,1]
	s_waitcnt vmcnt(9)
	s_nop 0
	v_mov_b32_dpp v32, v36 row_shr:1 row_mask:0xf bank_mask:0xf
	v_mov_b32_dpp v33, v37 row_shr:1 row_mask:0xf bank_mask:0xf
	v_mov_b32_dpp v38, v34 row_shl:1 row_mask:0xf bank_mask:0xf
	v_mov_b32_dpp v39, v35 row_shl:1 row_mask:0xf bank_mask:0xf
	v_pk_mul_f32 v[34:35], v[34:35], s[32:33]
	v_pk_mul_f32 v[36:37], v[36:37], s[32:33]
	v_cndmask_b32_e64 v33, v33, v32, vcc
	v_cndmask_b32_e64 v38, v38, v39, s[16:17]
	v_pk_mul_f32 v[84:85], v[34:35], s[30:31]
	v_pk_mul_f32 v[86:87], v[36:37], s[30:31]
	v_pk_mul_f32 v[32:33], v[32:33], s[32:33]
	v_pk_mul_f32 v[38:39], v[38:39], s[32:33]
	v_pk_add_f32 v[96:97], v[34:35], v[16:17] neg_lo:[0,1] neg_hi:[0,1]
	v_pk_add_f32 v[98:99], v[32:33], v[18:19] neg_lo:[0,1] neg_hi:[0,1]
	v_pk_add_f32 v[100:101], v[34:35], v[18:19] neg_lo:[0,1] neg_hi:[0,1]
	v_pk_add_f32 v[102:103], v[36:37], v[18:19] neg_lo:[0,1] neg_hi:[0,1]
	v_pk_add_f32 v[104:105], v[34:35], v[20:21] neg_lo:[0,1] neg_hi:[0,1]
	v_pk_add_f32 v[106:107], v[36:37], v[20:21] neg_lo:[0,1] neg_hi:[0,1]
	v_pk_add_f32 v[108:109], v[38:39], v[20:21] neg_lo:[0,1] neg_hi:[0,1]
	v_pk_add_f32 v[110:111], v[36:37], v[22:23] neg_lo:[0,1] neg_hi:[0,1]
	v_pk_fma_f32 v[96:97], v[96:97], v[96:97], s[28:29] neg_lo:[1,0,0] neg_hi:[1,0,0]
	v_pk_fma_f32 v[98:99], v[98:99], v[98:99], s[28:29] neg_lo:[1,0,0] neg_hi:[1,0,0]
	v_pk_fma_f32 v[100:101], v[100:101], v[100:101], s[22:23] neg_lo:[1,0,0] neg_hi:[1,0,0]
	v_pk_fma_f32 v[102:103], v[102:103], v[102:103], s[28:29] neg_lo:[1,0,0] neg_hi:[1,0,0]
	v_pk_fma_f32 v[104:105], v[104:105], v[104:105], s[28:29] neg_lo:[1,0,0] neg_hi:[1,0,0]
	v_pk_fma_f32 v[106:107], v[106:107], v[106:107], s[22:23] neg_lo:[1,0,0] neg_hi:[1,0,0]
	v_pk_fma_f32 v[108:109], v[108:109], v[108:109], s[28:29] neg_lo:[1,0,0] neg_hi:[1,0,0]
	v_pk_fma_f32 v[110:111], v[110:111], v[110:111], s[28:29] neg_lo:[1,0,0] neg_hi:[1,0,0]
	v_exp_f32_e32 v96, v96
	v_exp_f32_e32 v97, v97
	v_exp_f32_e32 v98, v98
	v_exp_f32_e32 v99, v99
	v_exp_f32_e32 v100, v100
	v_exp_f32_e32 v101, v101
	v_exp_f32_e32 v102, v102
	v_exp_f32_e32 v103, v103
	v_exp_f32_e32 v104, v104
	v_exp_f32_e32 v105, v105
	v_exp_f32_e32 v106, v106
	v_exp_f32_e32 v107, v107
	v_exp_f32_e32 v108, v108
	v_exp_f32_e32 v109, v109
	v_exp_f32_e32 v110, v110
	v_exp_f32_e32 v111, v111
	v_pk_add_f32 v[112:113], v[34:35], v[18:19] op_sel:[1,0] op_sel_hi:[0,1] neg_lo:[0,1] neg_hi:[0,1]
	v_pk_add_f32 v[114:115], v[36:37], v[20:21] op_sel:[1,0] op_sel_hi:[0,1] neg_lo:[0,1] neg_hi:[0,1]
	v_pk_add_f32 v[116:117], v[34:35], v[24:25] neg_lo:[0,1] neg_hi:[0,1]
	v_pk_add_f32 v[118:119], v[32:33], v[26:27] neg_lo:[0,1] neg_hi:[0,1]
	v_pk_add_f32 v[120:121], v[34:35], v[26:27] neg_lo:[0,1] neg_hi:[0,1]
	v_pk_add_f32 v[122:123], v[36:37], v[26:27] neg_lo:[0,1] neg_hi:[0,1]
	v_pk_add_f32 v[124:125], v[34:35], v[28:29] neg_lo:[0,1] neg_hi:[0,1]
	v_pk_add_f32 v[126:127], v[36:37], v[28:29] neg_lo:[0,1] neg_hi:[0,1]
	v_pk_fma_f32 v[112:113], v[112:113], v[112:113], s[26:27] neg_lo:[1,0,0] neg_hi:[1,0,0]
	v_pk_fma_f32 v[114:115], v[114:115], v[114:115], s[26:27] neg_lo:[1,0,0] neg_hi:[1,0,0]
	v_pk_fma_f32 v[116:117], v[116:117], v[116:117], s[26:27] neg_lo:[1,0,0] neg_hi:[1,0,0]
	v_pk_fma_f32 v[118:119], v[118:119], v[118:119], s[26:27] neg_lo:[1,0,0] neg_hi:[1,0,0]
	v_pk_fma_f32 v[120:121], v[120:121], v[120:121], s[20:21] neg_lo:[1,0,0] neg_hi:[1,0,0]
	v_pk_fma_f32 v[122:123], v[122:123], v[122:123], s[26:27] neg_lo:[1,0,0] neg_hi:[1,0,0]
	v_pk_fma_f32 v[124:125], v[124:125], v[124:125], s[26:27] neg_lo:[1,0,0] neg_hi:[1,0,0]
	v_pk_fma_f32 v[126:127], v[126:127], v[126:127], s[20:21] neg_lo:[1,0,0] neg_hi:[1,0,0]
	v_exp_f32_e32 v112, v112
	v_exp_f32_e32 v113, v113
	v_exp_f32_e32 v114, v114
	v_exp_f32_e32 v115, v115
	v_exp_f32_e32 v116, v116
	v_exp_f32_e32 v117, v117
	v_exp_f32_e32 v118, v118
	v_exp_f32_e32 v119, v119
	v_exp_f32_e32 v120, v120
	v_exp_f32_e32 v121, v121
	v_exp_f32_e32 v122, v122
	v_exp_f32_e32 v123, v123
	v_exp_f32_e32 v124, v124
	v_exp_f32_e32 v125, v125
	v_exp_f32_e32 v126, v126
	v_exp_f32_e32 v127, v127
	v_pk_add_f32 v[80:81], s[30:31], v[96:97]
	v_pk_fma_f32 v[84:85], v[96:97], v[16:17], v[84:85]
	v_pk_add_f32 v[64:65], v[64:65], v[98:99]
	v_pk_fma_f32 v[68:69], v[98:99], v[32:33], v[68:69]
	v_pk_add_f32 v[80:81], v[80:81], v[100:101]
	v_pk_add_f32 v[64:65], v[64:65], v[100:101]
	v_pk_fma_f32 v[68:69], v[100:101], v[34:35], v[68:69]
	v_pk_fma_f32 v[84:85], v[100:101], v[18:19], v[84:85]
	v_pk_add_f32 v[64:65], v[64:65], v[102:103]
	v_pk_fma_f32 v[68:69], v[102:103], v[36:37], v[68:69]
	v_pk_add_f32 v[82:83], s[30:31], v[102:103]
	v_pk_fma_f32 v[86:87], v[102:103], v[18:19], v[86:87]
	v_pk_add_f32 v[66:67], v[66:67], v[104:105]
	v_pk_fma_f32 v[70:71], v[104:105], v[34:35], v[70:71]
	v_pk_add_f32 v[80:81], v[80:81], v[104:105]
	v_pk_fma_f32 v[84:85], v[104:105], v[20:21], v[84:85]
	v_pk_add_f32 v[66:67], v[66:67], v[106:107]
	v_pk_fma_f32 v[70:71], v[106:107], v[36:37], v[70:71]
	v_pk_add_f32 v[82:83], v[82:83], v[106:107]
	v_pk_fma_f32 v[86:87], v[106:107], v[20:21], v[86:87]
	v_pk_add_f32 v[66:67], v[66:67], v[108:109]
	v_pk_fma_f32 v[70:71], v[108:109], v[38:39], v[70:71]
	v_pk_add_f32 v[82:83], v[82:83], v[110:111]
	v_pk_fma_f32 v[86:87], v[110:111], v[22:23], v[86:87]
	v_pk_add_f32 v[96:97], v[38:39], v[28:29] neg_lo:[0,1] neg_hi:[0,1]
	v_pk_add_f32 v[98:99], v[36:37], v[30:31] neg_lo:[0,1] neg_hi:[0,1]
	v_pk_add_f32 v[100:101], v[34:35], v[26:27] op_sel:[1,0] op_sel_hi:[0,1] neg_lo:[0,1] neg_hi:[0,1]
	v_pk_add_f32 v[102:103], v[36:37], v[28:29] op_sel:[1,0] op_sel_hi:[0,1] neg_lo:[0,1] neg_hi:[0,1]
	v_pk_add_f32 v[104:105], v[34:35], v[32:33] neg_lo:[0,1] neg_hi:[0,1]
	v_pk_add_f32 v[106:107], v[36:37], v[34:35] neg_lo:[0,1] neg_hi:[0,1]
	v_pk_add_f32 v[108:109], v[38:39], v[36:37] neg_lo:[0,1] neg_hi:[0,1]
	v_pk_fma_f32 v[96:97], v[96:97], v[96:97], s[26:27] neg_lo:[1,0,0] neg_hi:[1,0,0]
	v_pk_fma_f32 v[98:99], v[98:99], v[98:99], s[26:27] neg_lo:[1,0,0] neg_hi:[1,0,0]
	v_pk_fma_f32 v[100:101], v[100:101], v[100:101], s[24:25] neg_lo:[1,0,0] neg_hi:[1,0,0]
	v_pk_fma_f32 v[102:103], v[102:103], v[102:103], s[24:25] neg_lo:[1,0,0] neg_hi:[1,0,0]
	v_pk_fma_f32 v[104:105], v[104:105], v[104:105], s[22:23] neg_lo:[1,0,0] neg_hi:[1,0,0]
	v_pk_fma_f32 v[106:107], v[106:107], v[106:107], s[22:23] neg_lo:[1,0,0] neg_hi:[1,0,0]
	v_pk_fma_f32 v[108:109], v[108:109], v[108:109], s[22:23] neg_lo:[1,0,0] neg_hi:[1,0,0]
	v_exp_f32_e32 v96, v96
	v_exp_f32_e32 v97, v97
	v_exp_f32_e32 v98, v98
	v_exp_f32_e32 v99, v99
	v_exp_f32_e32 v100, v100
	v_exp_f32_e32 v101, v101
	v_exp_f32_e32 v102, v102
	v_exp_f32_e32 v103, v103
	v_exp_f32_e32 v104, v104
	v_exp_f32_e32 v105, v105
	v_exp_f32_e32 v106, v106
	v_exp_f32_e32 v107, v107
	v_exp_f32_e32 v108, v108
	v_exp_f32_e32 v109, v109
	v_pk_add_f32 v[64:65], v[64:65], v[112:113]
	v_pk_fma_f32 v[68:69], v[112:113], v[34:35], v[68:69] op_sel:[0,1,0] op_sel_hi:[1,0,1]
	v_pk_add_f32 v[80:81], v[80:81], v[112:113] op_sel:[0,1] op_sel_hi:[1,0]
	v_pk_fma_f32 v[84:85], v[112:113], v[18:19], v[84:85] op_sel:[1,1,0] op_sel_hi:[0,0,1]
	v_pk_add_f32 v[66:67], v[66:67], v[114:115]
	v_pk_fma_f32 v[70:71], v[114:115], v[36:37], v[70:71] op_sel:[0,1,0] op_sel_hi:[1,0,1]
	v_pk_add_f32 v[82:83], v[82:83], v[114:115] op_sel:[0,1] op_sel_hi:[1,0]
	v_pk_fma_f32 v[86:87], v[114:115], v[20:21], v[86:87] op_sel:[1,1,0] op_sel_hi:[0,0,1]
	v_pk_add_f32 v[80:81], v[80:81], v[116:117]
	v_pk_fma_f32 v[84:85], v[116:117], v[24:25], v[84:85]
	v_pk_add_f32 v[72:73], v[72:73], v[118:119]
	v_pk_fma_f32 v[76:77], v[118:119], v[32:33], v[76:77]
	v_pk_add_f32 v[80:81], v[80:81], v[120:121]
	v_pk_add_f32 v[72:73], v[72:73], v[120:121]
	v_pk_fma_f32 v[76:77], v[120:121], v[34:35], v[76:77]
	v_pk_fma_f32 v[84:85], v[120:121], v[26:27], v[84:85]
	v_pk_add_f32 v[72:73], v[72:73], v[122:123]
	v_pk_fma_f32 v[76:77], v[122:123], v[36:37], v[76:77]
	v_pk_add_f32 v[82:83], v[82:83], v[122:123]
	v_pk_fma_f32 v[86:87], v[122:123], v[26:27], v[86:87]
	v_pk_add_f32 v[74:75], v[74:75], v[124:125]
	v_pk_fma_f32 v[78:79], v[124:125], v[34:35], v[78:79]
	v_pk_add_f32 v[80:81], v[80:81], v[124:125]
	v_pk_fma_f32 v[84:85], v[124:125], v[28:29], v[84:85]
	v_pk_add_f32 v[74:75], v[74:75], v[126:127]
	v_pk_fma_f32 v[78:79], v[126:127], v[36:37], v[78:79]
	v_pk_add_f32 v[82:83], v[82:83], v[126:127]
	v_pk_fma_f32 v[86:87], v[126:127], v[28:29], v[86:87]
	v_sub_f32_e32 v116, v34, v17
	v_sub_f32_e32 v118, v33, v18
	v_sub_f32_e32 v120, v36, v19
	v_sub_f32_e32 v122, v35, v20
	v_sub_f32_e32 v124, v38, v21
	v_sub_f32_e32 v126, v37, v22
	v_sub_f32_e32 v113, v34, v25
	v_sub_f32_e32 v115, v33, v26
	v_sub_f32_e32 v117, v36, v27
	v_sub_f32_e32 v119, v35, v28
	v_sub_f32_e32 v121, v38, v29
	v_sub_f32_e32 v123, v37, v30
	v_sub_f32_e32 v125, v34, v33
	v_sub_f32_e32 v112, v35, v34
	v_sub_f32_e32 v127, v36, v35
	v_sub_f32_e32 v114, v37, v36
	v_fma_f32 v116, -v116, v116, s26
	v_fma_f32 v118, -v118, v118, s26
	v_fma_f32 v120, -v120, v120, s26
	v_fma_f32 v122, -v122, v122, s26
	v_fma_f32 v124, -v124, v124, s26
	v_fma_f32 v126, -v126, v126, s26
	v_fma_f32 v113, -v113, v113, s24
	v_fma_f32 v115, -v115, v115, s24
	v_fma_f32 v117, -v117, v117, s24
	v_fma_f32 v119, -v119, v119, s24
	v_fma_f32 v121, -v121, v121, s24
	v_fma_f32 v123, -v123, v123, s24
	v_fma_f32 v125, -v125, v125, s20
	v_fma_f32 v112, -v112, v112, s20
	v_fma_f32 v127, -v127, v127, s20
	v_fma_f32 v114, -v114, v114, s20
	v_exp_f32_e32 v116, v116
	v_exp_f32_e32 v118, v118
	v_exp_f32_e32 v120, v120
	v_exp_f32_e32 v122, v122
	v_exp_f32_e32 v124, v124
	v_exp_f32_e32 v126, v126
	v_exp_f32_e32 v113, v113
	v_exp_f32_e32 v115, v115
	v_exp_f32_e32 v117, v117
	v_exp_f32_e32 v119, v119
	v_exp_f32_e32 v121, v121
	v_exp_f32_e32 v123, v123
	v_exp_f32_e32 v125, v125
	v_exp_f32_e32 v112, v112
	v_exp_f32_e32 v127, v127
	v_exp_f32_e32 v114, v114
	v_pk_add_f32 v[74:75], v[74:75], v[96:97]
	v_pk_fma_f32 v[78:79], v[96:97], v[38:39], v[78:79]
	v_pk_add_f32 v[82:83], v[82:83], v[98:99]
	v_pk_fma_f32 v[86:87], v[98:99], v[30:31], v[86:87]
	v_pk_add_f32 v[72:73], v[72:73], v[100:101]
	v_pk_fma_f32 v[76:77], v[100:101], v[34:35], v[76:77] op_sel:[0,1,0] op_sel_hi:[1,0,1]
	v_pk_add_f32 v[80:81], v[80:81], v[100:101] op_sel:[0,1] op_sel_hi:[1,0]
	v_pk_fma_f32 v[84:85], v[100:101], v[26:27], v[84:85] op_sel:[1,1,0] op_sel_hi:[0,0,1]
	v_pk_add_f32 v[74:75], v[74:75], v[102:103]
	v_pk_fma_f32 v[78:79], v[102:103], v[36:37], v[78:79] op_sel:[0,1,0] op_sel_hi:[1,0,1]
	v_pk_add_f32 v[82:83], v[82:83], v[102:103] op_sel:[0,1] op_sel_hi:[1,0]
	v_pk_fma_f32 v[86:87], v[102:103], v[28:29], v[86:87] op_sel:[1,1,0] op_sel_hi:[0,0,1]
	v_pk_add_f32 v[80:81], v[80:81], v[104:105]
	v_pk_fma_f32 v[84:85], v[104:105], v[32:33], v[84:85]
	v_pk_add_f32 v[82:83], v[82:83], v[106:107]
	v_pk_add_f32 v[80:81], v[80:81], v[106:107]
	v_pk_fma_f32 v[84:85], v[106:107], v[36:37], v[84:85]
	v_pk_fma_f32 v[86:87], v[106:107], v[34:35], v[86:87]
	v_pk_add_f32 v[82:83], v[82:83], v[108:109]
	v_pk_fma_f32 v[86:87], v[108:109], v[38:39], v[86:87]
	v_sub_f32_e64 v96, v38, v37
	v_fma_f32 v96, -v96, v96, s20
	s_nop 0
	v_exp_f32_e32 v96, v96
	v_add_f32_e32 v80, v80, v116
	v_fmac_f32_e32 v84, v116, v17
	v_add_f32_e32 v64, v64, v118
	v_fmac_f32_e32 v68, v118, v33
	v_add_f32_e32 v65, v65, v120
	v_fmac_f32_e32 v69, v120, v36
	v_add_f32_e32 v82, v82, v120
	v_fmac_f32_e32 v86, v120, v19
	v_add_f32_e32 v66, v66, v122
	v_fmac_f32_e32 v70, v122, v35
	v_add_f32_e32 v81, v81, v122
	v_fmac_f32_e32 v85, v122, v20
	v_add_f32_e32 v67, v67, v124
	v_fmac_f32_e32 v71, v124, v38
	v_add_f32_e32 v83, v83, v126
	v_fmac_f32_e32 v87, v126, v22
	v_add_f32_e32 v80, v80, v113
	v_fmac_f32_e32 v84, v113, v25
	v_add_f32_e32 v72, v72, v115
	v_fmac_f32_e32 v76, v115, v33
	v_add_f32_e32 v73, v73, v117
	v_fmac_f32_e32 v77, v117, v36
	v_add_f32_e32 v82, v82, v117
	v_fmac_f32_e32 v86, v117, v27
	v_add_f32_e32 v74, v74, v119
	v_fmac_f32_e32 v78, v119, v35
	v_add_f32_e32 v81, v81, v119
	v_fmac_f32_e32 v85, v119, v28
	v_add_f32_e32 v75, v75, v121
	v_fmac_f32_e32 v79, v121, v38
	v_add_f32_e32 v83, v83, v123
	v_fmac_f32_e32 v87, v123, v30
	v_add_f32_e32 v80, v80, v125
	v_fmac_f32_e32 v84, v125, v33
	v_add_f32_e32 v81, v81, v127
	v_fmac_f32_e32 v85, v127, v36
	v_add_f32_e32 v82, v82, v127
	v_fmac_f32_e32 v86, v127, v35
	v_pk_add_f32 v[80:81], v[80:81], v[112:113] op_sel_hi:[1,0]
	v_pk_fma_f32 v[84:85], v[112:113], v[34:35], v[84:85] op_sel:[0,1,0] op_sel_hi:[0,0,1]
	v_pk_add_f32 v[82:83], v[82:83], v[114:115] op_sel_hi:[1,0]
	v_pk_fma_f32 v[86:87], v[114:115], v[36:37], v[86:87] op_sel:[0,1,0] op_sel_hi:[0,0,1]
	s_nop 0
	v_add_f32_e32 v83, v83, v96
	v_fmac_f32_e32 v87, v96, v38
	v_rcp_f32_e32 v96, v64
	v_rcp_f32_e32 v97, v65
	v_rcp_f32_e32 v98, v66
	v_rcp_f32_e64 v99, v67
	v_pk_mul_f32 v[68:69], v[68:69], s[34:35]
	v_pk_mul_f32 v[70:71], v[70:71], s[34:35]
	v_pk_mul_f32 v[68:69], v[68:69], v[96:97]
	v_pk_mul_f32 v[70:71], v[70:71], v[98:99]
	buffer_store_dwordx4 v[68:71], v130, s[12:15], 0 offen sc1
	s_waitcnt vmcnt(7)
	s_nop 0
	v_mov_b32_dpp v40, v44 row_shr:1 row_mask:0xf bank_mask:0xf
	v_mov_b32_dpp v41, v45 row_shr:1 row_mask:0xf bank_mask:0xf
	v_mov_b32_dpp v46, v42 row_shl:1 row_mask:0xf bank_mask:0xf
	v_mov_b32_dpp v47, v43 row_shl:1 row_mask:0xf bank_mask:0xf
	v_pk_mul_f32 v[42:43], v[42:43], s[32:33]
	v_pk_mul_f32 v[44:45], v[44:45], s[32:33]
	v_cndmask_b32_e64 v41, v41, v40, vcc
	v_cndmask_b32_e64 v46, v46, v47, s[16:17]
	v_pk_mul_f32 v[92:93], v[42:43], s[30:31]
	v_pk_mul_f32 v[94:95], v[44:45], s[30:31]
	v_pk_mul_f32 v[40:41], v[40:41], s[32:33]
	v_pk_mul_f32 v[46:47], v[46:47], s[32:33]
	v_pk_add_f32 v[96:97], v[42:43], v[24:25] neg_lo:[0,1] neg_hi:[0,1]
	v_pk_add_f32 v[98:99], v[40:41], v[26:27] neg_lo:[0,1] neg_hi:[0,1]
	v_pk_add_f32 v[100:101], v[42:43], v[26:27] neg_lo:[0,1] neg_hi:[0,1]
	v_pk_add_f32 v[102:103], v[44:45], v[26:27] neg_lo:[0,1] neg_hi:[0,1]
	v_pk_add_f32 v[104:105], v[42:43], v[28:29] neg_lo:[0,1] neg_hi:[0,1]
	v_pk_add_f32 v[106:107], v[44:45], v[28:29] neg_lo:[0,1] neg_hi:[0,1]
	v_pk_add_f32 v[108:109], v[46:47], v[28:29] neg_lo:[0,1] neg_hi:[0,1]
	v_pk_add_f32 v[110:111], v[44:45], v[30:31] neg_lo:[0,1] neg_hi:[0,1]
	v_pk_fma_f32 v[96:97], v[96:97], v[96:97], s[28:29] neg_lo:[1,0,0] neg_hi:[1,0,0]
	v_pk_fma_f32 v[98:99], v[98:99], v[98:99], s[28:29] neg_lo:[1,0,0] neg_hi:[1,0,0]
	v_pk_fma_f32 v[100:101], v[100:101], v[100:101], s[22:23] neg_lo:[1,0,0] neg_hi:[1,0,0]
	v_pk_fma_f32 v[102:103], v[102:103], v[102:103], s[28:29] neg_lo:[1,0,0] neg_hi:[1,0,0]
	v_pk_fma_f32 v[104:105], v[104:105], v[104:105], s[28:29] neg_lo:[1,0,0] neg_hi:[1,0,0]
	v_pk_fma_f32 v[106:107], v[106:107], v[106:107], s[22:23] neg_lo:[1,0,0] neg_hi:[1,0,0]
	v_pk_fma_f32 v[108:109], v[108:109], v[108:109], s[28:29] neg_lo:[1,0,0] neg_hi:[1,0,0]
	v_pk_fma_f32 v[110:111], v[110:111], v[110:111], s[28:29] neg_lo:[1,0,0] neg_hi:[1,0,0]
	v_exp_f32_e32 v96, v96
	v_exp_f32_e32 v97, v97
	v_exp_f32_e32 v98, v98
	v_exp_f32_e32 v99, v99
	v_exp_f32_e32 v100, v100
	v_exp_f32_e32 v101, v101
	v_exp_f32_e32 v102, v102
	v_exp_f32_e32 v103, v103
	v_exp_f32_e32 v104, v104
	v_exp_f32_e32 v105, v105
	v_exp_f32_e32 v106, v106
	v_exp_f32_e32 v107, v107
	v_exp_f32_e32 v108, v108
	v_exp_f32_e32 v109, v109
	v_exp_f32_e32 v110, v110
	v_exp_f32_e32 v111, v111
	v_pk_add_f32 v[112:113], v[42:43], v[26:27] op_sel:[1,0] op_sel_hi:[0,1] neg_lo:[0,1] neg_hi:[0,1]
	v_pk_add_f32 v[114:115], v[44:45], v[28:29] op_sel:[1,0] op_sel_hi:[0,1] neg_lo:[0,1] neg_hi:[0,1]
	v_pk_add_f32 v[116:117], v[42:43], v[32:33] neg_lo:[0,1] neg_hi:[0,1]
	v_pk_add_f32 v[118:119], v[40:41], v[34:35] neg_lo:[0,1] neg_hi:[0,1]
	v_pk_add_f32 v[120:121], v[42:43], v[34:35] neg_lo:[0,1] neg_hi:[0,1]
	v_pk_add_f32 v[122:123], v[44:45], v[34:35] neg_lo:[0,1] neg_hi:[0,1]
	v_pk_add_f32 v[124:125], v[42:43], v[36:37] neg_lo:[0,1] neg_hi:[0,1]
	v_pk_add_f32 v[126:127], v[44:45], v[36:37] neg_lo:[0,1] neg_hi:[0,1]
	v_pk_fma_f32 v[112:113], v[112:113], v[112:113], s[26:27] neg_lo:[1,0,0] neg_hi:[1,0,0]
	v_pk_fma_f32 v[114:115], v[114:115], v[114:115], s[26:27] neg_lo:[1,0,0] neg_hi:[1,0,0]
	v_pk_fma_f32 v[116:117], v[116:117], v[116:117], s[26:27] neg_lo:[1,0,0] neg_hi:[1,0,0]
	v_pk_fma_f32 v[118:119], v[118:119], v[118:119], s[26:27] neg_lo:[1,0,0] neg_hi:[1,0,0]
	v_pk_fma_f32 v[120:121], v[120:121], v[120:121], s[20:21] neg_lo:[1,0,0] neg_hi:[1,0,0]
	v_pk_fma_f32 v[122:123], v[122:123], v[122:123], s[26:27] neg_lo:[1,0,0] neg_hi:[1,0,0]
	v_pk_fma_f32 v[124:125], v[124:125], v[124:125], s[26:27] neg_lo:[1,0,0] neg_hi:[1,0,0]
	v_pk_fma_f32 v[126:127], v[126:127], v[126:127], s[20:21] neg_lo:[1,0,0] neg_hi:[1,0,0]
	v_exp_f32_e32 v112, v112
	v_exp_f32_e32 v113, v113
	v_exp_f32_e32 v114, v114
	v_exp_f32_e32 v115, v115
	v_exp_f32_e32 v116, v116
	v_exp_f32_e32 v117, v117
	v_exp_f32_e32 v118, v118
	v_exp_f32_e32 v119, v119
	v_exp_f32_e32 v120, v120
	v_exp_f32_e32 v121, v121
	v_exp_f32_e32 v122, v122
	v_exp_f32_e32 v123, v123
	v_exp_f32_e32 v124, v124
	v_exp_f32_e32 v125, v125
	v_exp_f32_e32 v126, v126
	v_exp_f32_e32 v127, v127
	v_pk_add_f32 v[88:89], s[30:31], v[96:97]
	v_pk_fma_f32 v[92:93], v[96:97], v[24:25], v[92:93]
	v_pk_add_f32 v[72:73], v[72:73], v[98:99]
	v_pk_fma_f32 v[76:77], v[98:99], v[40:41], v[76:77]
	v_pk_add_f32 v[88:89], v[88:89], v[100:101]
	v_pk_add_f32 v[72:73], v[72:73], v[100:101]
	v_pk_fma_f32 v[76:77], v[100:101], v[42:43], v[76:77]
	v_pk_fma_f32 v[92:93], v[100:101], v[26:27], v[92:93]
	v_pk_add_f32 v[72:73], v[72:73], v[102:103]
	v_pk_fma_f32 v[76:77], v[102:103], v[44:45], v[76:77]
	v_pk_add_f32 v[90:91], s[30:31], v[102:103]
	v_pk_fma_f32 v[94:95], v[102:103], v[26:27], v[94:95]
	v_pk_add_f32 v[74:75], v[74:75], v[104:105]
	v_pk_fma_f32 v[78:79], v[104:105], v[42:43], v[78:79]
	v_pk_add_f32 v[88:89], v[88:89], v[104:105]
	v_pk_fma_f32 v[92:93], v[104:105], v[28:29], v[92:93]
	v_pk_add_f32 v[74:75], v[74:75], v[106:107]
	v_pk_fma_f32 v[78:79], v[106:107], v[44:45], v[78:79]
	v_pk_add_f32 v[90:91], v[90:91], v[106:107]
	v_pk_fma_f32 v[94:95], v[106:107], v[28:29], v[94:95]
	v_pk_add_f32 v[74:75], v[74:75], v[108:109]
	v_pk_fma_f32 v[78:79], v[108:109], v[46:47], v[78:79]
	v_pk_add_f32 v[90:91], v[90:91], v[110:111]
	v_pk_fma_f32 v[94:95], v[110:111], v[30:31], v[94:95]
	v_pk_add_f32 v[96:97], v[46:47], v[36:37] neg_lo:[0,1] neg_hi:[0,1]
	v_pk_add_f32 v[98:99], v[44:45], v[38:39] neg_lo:[0,1] neg_hi:[0,1]
	v_pk_add_f32 v[100:101], v[42:43], v[34:35] op_sel:[1,0] op_sel_hi:[0,1] neg_lo:[0,1] neg_hi:[0,1]
	v_pk_add_f32 v[102:103], v[44:45], v[36:37] op_sel:[1,0] op_sel_hi:[0,1] neg_lo:[0,1] neg_hi:[0,1]
	v_pk_add_f32 v[104:105], v[42:43], v[40:41] neg_lo:[0,1] neg_hi:[0,1]
	v_pk_add_f32 v[106:107], v[44:45], v[42:43] neg_lo:[0,1] neg_hi:[0,1]
	v_pk_add_f32 v[108:109], v[46:47], v[44:45] neg_lo:[0,1] neg_hi:[0,1]
	v_pk_fma_f32 v[96:97], v[96:97], v[96:97], s[26:27] neg_lo:[1,0,0] neg_hi:[1,0,0]
	v_pk_fma_f32 v[98:99], v[98:99], v[98:99], s[26:27] neg_lo:[1,0,0] neg_hi:[1,0,0]
	v_pk_fma_f32 v[100:101], v[100:101], v[100:101], s[24:25] neg_lo:[1,0,0] neg_hi:[1,0,0]
	v_pk_fma_f32 v[102:103], v[102:103], v[102:103], s[24:25] neg_lo:[1,0,0] neg_hi:[1,0,0]
	v_pk_fma_f32 v[104:105], v[104:105], v[104:105], s[22:23] neg_lo:[1,0,0] neg_hi:[1,0,0]
	v_pk_fma_f32 v[106:107], v[106:107], v[106:107], s[22:23] neg_lo:[1,0,0] neg_hi:[1,0,0]
	v_pk_fma_f32 v[108:109], v[108:109], v[108:109], s[22:23] neg_lo:[1,0,0] neg_hi:[1,0,0]
	v_exp_f32_e32 v96, v96
	v_exp_f32_e32 v97, v97
	v_exp_f32_e32 v98, v98
	v_exp_f32_e32 v99, v99
	v_exp_f32_e32 v100, v100
	v_exp_f32_e32 v101, v101
	v_exp_f32_e32 v102, v102
	v_exp_f32_e32 v103, v103
	v_exp_f32_e32 v104, v104
	v_exp_f32_e32 v105, v105
	v_exp_f32_e32 v106, v106
	v_exp_f32_e32 v107, v107
	v_exp_f32_e32 v108, v108
	v_exp_f32_e32 v109, v109
	v_pk_add_f32 v[72:73], v[72:73], v[112:113]
	v_pk_fma_f32 v[76:77], v[112:113], v[42:43], v[76:77] op_sel:[0,1,0] op_sel_hi:[1,0,1]
	v_pk_add_f32 v[88:89], v[88:89], v[112:113] op_sel:[0,1] op_sel_hi:[1,0]
	v_pk_fma_f32 v[92:93], v[112:113], v[26:27], v[92:93] op_sel:[1,1,0] op_sel_hi:[0,0,1]
	v_pk_add_f32 v[74:75], v[74:75], v[114:115]
	v_pk_fma_f32 v[78:79], v[114:115], v[44:45], v[78:79] op_sel:[0,1,0] op_sel_hi:[1,0,1]
	v_pk_add_f32 v[90:91], v[90:91], v[114:115] op_sel:[0,1] op_sel_hi:[1,0]
	v_pk_fma_f32 v[94:95], v[114:115], v[28:29], v[94:95] op_sel:[1,1,0] op_sel_hi:[0,0,1]
	v_pk_add_f32 v[88:89], v[88:89], v[116:117]
	v_pk_fma_f32 v[92:93], v[116:117], v[32:33], v[92:93]
	v_pk_add_f32 v[80:81], v[80:81], v[118:119]
	v_pk_fma_f32 v[84:85], v[118:119], v[40:41], v[84:85]
	v_pk_add_f32 v[88:89], v[88:89], v[120:121]
	v_pk_add_f32 v[80:81], v[80:81], v[120:121]
	v_pk_fma_f32 v[84:85], v[120:121], v[42:43], v[84:85]
	v_pk_fma_f32 v[92:93], v[120:121], v[34:35], v[92:93]
	v_pk_add_f32 v[80:81], v[80:81], v[122:123]
	v_pk_fma_f32 v[84:85], v[122:123], v[44:45], v[84:85]
	v_pk_add_f32 v[90:91], v[90:91], v[122:123]
	v_pk_fma_f32 v[94:95], v[122:123], v[34:35], v[94:95]
	v_pk_add_f32 v[82:83], v[82:83], v[124:125]
	v_pk_fma_f32 v[86:87], v[124:125], v[42:43], v[86:87]
	v_pk_add_f32 v[88:89], v[88:89], v[124:125]
	v_pk_fma_f32 v[92:93], v[124:125], v[36:37], v[92:93]
	v_pk_add_f32 v[82:83], v[82:83], v[126:127]
	v_pk_fma_f32 v[86:87], v[126:127], v[44:45], v[86:87]
	v_pk_add_f32 v[90:91], v[90:91], v[126:127]
	v_pk_fma_f32 v[94:95], v[126:127], v[36:37], v[94:95]
	v_sub_f32_e32 v116, v42, v25
	v_sub_f32_e32 v118, v41, v26
	v_sub_f32_e32 v120, v44, v27
	v_sub_f32_e32 v122, v43, v28
	v_sub_f32_e32 v124, v46, v29
	v_sub_f32_e32 v126, v45, v30
	v_sub_f32_e32 v113, v42, v33
	v_sub_f32_e32 v115, v41, v34
	v_sub_f32_e32 v117, v44, v35
	v_sub_f32_e32 v119, v43, v36
	v_sub_f32_e32 v121, v46, v37
	v_sub_f32_e32 v123, v45, v38
	v_sub_f32_e32 v125, v42, v41
	v_sub_f32_e32 v112, v43, v42
	v_sub_f32_e32 v127, v44, v43
	v_sub_f32_e32 v114, v45, v44
	v_fma_f32 v116, -v116, v116, s26
	v_fma_f32 v118, -v118, v118, s26
	v_fma_f32 v120, -v120, v120, s26
	v_fma_f32 v122, -v122, v122, s26
	v_fma_f32 v124, -v124, v124, s26
	v_fma_f32 v126, -v126, v126, s26
	v_fma_f32 v113, -v113, v113, s24
	v_fma_f32 v115, -v115, v115, s24
	v_fma_f32 v117, -v117, v117, s24
	v_fma_f32 v119, -v119, v119, s24
	v_fma_f32 v121, -v121, v121, s24
	v_fma_f32 v123, -v123, v123, s24
	v_fma_f32 v125, -v125, v125, s20
	v_fma_f32 v112, -v112, v112, s20
	v_fma_f32 v127, -v127, v127, s20
	v_fma_f32 v114, -v114, v114, s20
	v_exp_f32_e32 v116, v116
	v_exp_f32_e32 v118, v118
	v_exp_f32_e32 v120, v120
	v_exp_f32_e32 v122, v122
	v_exp_f32_e32 v124, v124
	v_exp_f32_e32 v126, v126
	v_exp_f32_e32 v113, v113
	v_exp_f32_e32 v115, v115
	v_exp_f32_e32 v117, v117
	v_exp_f32_e32 v119, v119
	v_exp_f32_e32 v121, v121
	v_exp_f32_e32 v123, v123
	v_exp_f32_e32 v125, v125
	v_exp_f32_e32 v112, v112
	v_exp_f32_e32 v127, v127
	v_exp_f32_e32 v114, v114
	v_pk_add_f32 v[82:83], v[82:83], v[96:97]
	v_pk_fma_f32 v[86:87], v[96:97], v[46:47], v[86:87]
	v_pk_add_f32 v[90:91], v[90:91], v[98:99]
	v_pk_fma_f32 v[94:95], v[98:99], v[38:39], v[94:95]
	v_pk_add_f32 v[80:81], v[80:81], v[100:101]
	v_pk_fma_f32 v[84:85], v[100:101], v[42:43], v[84:85] op_sel:[0,1,0] op_sel_hi:[1,0,1]
	v_pk_add_f32 v[88:89], v[88:89], v[100:101] op_sel:[0,1] op_sel_hi:[1,0]
	v_pk_fma_f32 v[92:93], v[100:101], v[34:35], v[92:93] op_sel:[1,1,0] op_sel_hi:[0,0,1]
	v_pk_add_f32 v[82:83], v[82:83], v[102:103]
	v_pk_fma_f32 v[86:87], v[102:103], v[44:45], v[86:87] op_sel:[0,1,0] op_sel_hi:[1,0,1]
	v_pk_add_f32 v[90:91], v[90:91], v[102:103] op_sel:[0,1] op_sel_hi:[1,0]
	v_pk_fma_f32 v[94:95], v[102:103], v[36:37], v[94:95] op_sel:[1,1,0] op_sel_hi:[0,0,1]
	v_pk_add_f32 v[88:89], v[88:89], v[104:105]
	v_pk_fma_f32 v[92:93], v[104:105], v[40:41], v[92:93]
	v_pk_add_f32 v[90:91], v[90:91], v[106:107]
	v_pk_add_f32 v[88:89], v[88:89], v[106:107]
	v_pk_fma_f32 v[92:93], v[106:107], v[44:45], v[92:93]
	v_pk_fma_f32 v[94:95], v[106:107], v[42:43], v[94:95]
	v_pk_add_f32 v[90:91], v[90:91], v[108:109]
	v_pk_fma_f32 v[94:95], v[108:109], v[46:47], v[94:95]
	v_sub_f32_e64 v96, v46, v45
	v_fma_f32 v96, -v96, v96, s20
	s_nop 0
	v_exp_f32_e32 v96, v96
	v_add_f32_e32 v88, v88, v116
	v_fmac_f32_e32 v92, v116, v25
	v_add_f32_e32 v72, v72, v118
	v_fmac_f32_e32 v76, v118, v41
	v_add_f32_e32 v73, v73, v120
	v_fmac_f32_e32 v77, v120, v44
	v_add_f32_e32 v90, v90, v120
	v_fmac_f32_e32 v94, v120, v27
	v_add_f32_e32 v74, v74, v122
	v_fmac_f32_e32 v78, v122, v43
	v_add_f32_e32 v89, v89, v122
	v_fmac_f32_e32 v93, v122, v28
	v_add_f32_e32 v75, v75, v124
	v_fmac_f32_e32 v79, v124, v46
	v_add_f32_e32 v91, v91, v126
	v_fmac_f32_e32 v95, v126, v30
	v_add_f32_e32 v88, v88, v113
	v_fmac_f32_e32 v92, v113, v33
	v_add_f32_e32 v80, v80, v115
	v_fmac_f32_e32 v84, v115, v41
	v_add_f32_e32 v81, v81, v117
	v_fmac_f32_e32 v85, v117, v44
	v_add_f32_e32 v90, v90, v117
	v_fmac_f32_e32 v94, v117, v35
	v_add_f32_e32 v82, v82, v119
	v_fmac_f32_e32 v86, v119, v43
	v_add_f32_e32 v89, v89, v119
	v_fmac_f32_e32 v93, v119, v36
	v_add_f32_e32 v83, v83, v121
	v_fmac_f32_e32 v87, v121, v46
	v_add_f32_e32 v91, v91, v123
	v_fmac_f32_e32 v95, v123, v38
	v_add_f32_e32 v88, v88, v125
	v_fmac_f32_e32 v92, v125, v41
	v_add_f32_e32 v89, v89, v127
	v_fmac_f32_e32 v93, v127, v44
	v_add_f32_e32 v90, v90, v127
	v_fmac_f32_e32 v94, v127, v43
	v_pk_add_f32 v[88:89], v[88:89], v[112:113] op_sel_hi:[1,0]
	v_pk_fma_f32 v[92:93], v[112:113], v[42:43], v[92:93] op_sel:[0,1,0] op_sel_hi:[0,0,1]
	v_pk_add_f32 v[90:91], v[90:91], v[114:115] op_sel_hi:[1,0]
	v_pk_fma_f32 v[94:95], v[114:115], v[44:45], v[94:95] op_sel:[0,1,0] op_sel_hi:[0,0,1]
	s_nop 0
	v_add_f32_e32 v91, v91, v96
	v_fmac_f32_e32 v95, v96, v46
	v_rcp_f32_e32 v96, v72
	v_rcp_f32_e32 v97, v73
	v_rcp_f32_e32 v98, v74
	v_rcp_f32_e64 v99, v75
	v_pk_mul_f32 v[76:77], v[76:77], s[34:35]
	v_pk_mul_f32 v[78:79], v[78:79], s[34:35]
	v_pk_mul_f32 v[76:77], v[76:77], v[96:97]
	v_pk_mul_f32 v[78:79], v[78:79], v[98:99]
	buffer_store_dwordx4 v[76:79], v130, s[12:15], 0 offen offset:2048 sc1
	s_waitcnt vmcnt(5)
	s_nop 0
	v_mov_b32_dpp v48, v52 row_shr:1 row_mask:0xf bank_mask:0xf
	v_mov_b32_dpp v49, v53 row_shr:1 row_mask:0xf bank_mask:0xf
	v_mov_b32_dpp v54, v50 row_shl:1 row_mask:0xf bank_mask:0xf
	v_mov_b32_dpp v55, v51 row_shl:1 row_mask:0xf bank_mask:0xf
	v_pk_mul_f32 v[50:51], v[50:51], s[32:33]
	v_pk_mul_f32 v[52:53], v[52:53], s[32:33]
	v_cndmask_b32_e64 v49, v49, v48, vcc
	v_cndmask_b32_e64 v54, v54, v55, s[16:17]
	v_pk_mul_f32 v[48:49], v[48:49], s[32:33]
	v_pk_mul_f32 v[54:55], v[54:55], s[32:33]
	v_pk_add_f32 v[96:97], v[48:49], v[34:35] neg_lo:[0,1] neg_hi:[0,1]
	v_pk_add_f32 v[98:99], v[50:51], v[34:35] neg_lo:[0,1] neg_hi:[0,1]
	v_pk_add_f32 v[100:101], v[52:53], v[34:35] neg_lo:[0,1] neg_hi:[0,1]
	v_pk_add_f32 v[102:103], v[50:51], v[36:37] neg_lo:[0,1] neg_hi:[0,1]
	v_pk_add_f32 v[104:105], v[52:53], v[36:37] neg_lo:[0,1] neg_hi:[0,1]
	v_pk_add_f32 v[106:107], v[54:55], v[36:37] neg_lo:[0,1] neg_hi:[0,1]
	v_pk_add_f32 v[108:109], v[50:51], v[34:35] op_sel:[1,0] op_sel_hi:[0,1] neg_lo:[0,1] neg_hi:[0,1]
	v_pk_add_f32 v[110:111], v[52:53], v[36:37] op_sel:[1,0] op_sel_hi:[0,1] neg_lo:[0,1] neg_hi:[0,1]
	v_pk_fma_f32 v[96:97], v[96:97], v[96:97], s[28:29] neg_lo:[1,0,0] neg_hi:[1,0,0]
	v_pk_fma_f32 v[98:99], v[98:99], v[98:99], s[22:23] neg_lo:[1,0,0] neg_hi:[1,0,0]
	v_pk_fma_f32 v[100:101], v[100:101], v[100:101], s[28:29] neg_lo:[1,0,0] neg_hi:[1,0,0]
	v_pk_fma_f32 v[102:103], v[102:103], v[102:103], s[28:29] neg_lo:[1,0,0] neg_hi:[1,0,0]
	v_pk_fma_f32 v[104:105], v[104:105], v[104:105], s[22:23] neg_lo:[1,0,0] neg_hi:[1,0,0]
	v_pk_fma_f32 v[106:107], v[106:107], v[106:107], s[28:29] neg_lo:[1,0,0] neg_hi:[1,0,0]
	v_pk_fma_f32 v[108:109], v[108:109], v[108:109], s[26:27] neg_lo:[1,0,0] neg_hi:[1,0,0]
	v_pk_fma_f32 v[110:111], v[110:111], v[110:111], s[26:27] neg_lo:[1,0,0] neg_hi:[1,0,0]
	v_exp_f32_e32 v96, v96
	v_exp_f32_e32 v97, v97
	v_exp_f32_e32 v98, v98
	v_exp_f32_e32 v99, v99
	v_exp_f32_e32 v100, v100
	v_exp_f32_e32 v101, v101
	v_exp_f32_e32 v102, v102
	v_exp_f32_e32 v103, v103
	v_exp_f32_e32 v104, v104
	v_exp_f32_e32 v105, v105
	v_exp_f32_e32 v106, v106
	v_exp_f32_e32 v107, v107
	v_exp_f32_e32 v108, v108
	v_exp_f32_e32 v109, v109
	v_exp_f32_e32 v110, v110
	v_exp_f32_e32 v111, v111
	v_pk_add_f32 v[112:113], v[48:49], v[42:43] neg_lo:[0,1] neg_hi:[0,1]
	v_pk_add_f32 v[114:115], v[50:51], v[42:43] neg_lo:[0,1] neg_hi:[0,1]
	v_pk_add_f32 v[116:117], v[52:53], v[42:43] neg_lo:[0,1] neg_hi:[0,1]
	v_pk_add_f32 v[118:119], v[50:51], v[44:45] neg_lo:[0,1] neg_hi:[0,1]
	v_pk_add_f32 v[120:121], v[52:53], v[44:45] neg_lo:[0,1] neg_hi:[0,1]
	v_pk_add_f32 v[122:123], v[54:55], v[44:45] neg_lo:[0,1] neg_hi:[0,1]
	v_pk_add_f32 v[124:125], v[50:51], v[42:43] op_sel:[1,0] op_sel_hi:[0,1] neg_lo:[0,1] neg_hi:[0,1]
	v_pk_add_f32 v[126:127], v[52:53], v[44:45] op_sel:[1,0] op_sel_hi:[0,1] neg_lo:[0,1] neg_hi:[0,1]
	v_pk_fma_f32 v[112:113], v[112:113], v[112:113], s[26:27] neg_lo:[1,0,0] neg_hi:[1,0,0]
	v_pk_fma_f32 v[114:115], v[114:115], v[114:115], s[20:21] neg_lo:[1,0,0] neg_hi:[1,0,0]
	v_pk_fma_f32 v[116:117], v[116:117], v[116:117], s[26:27] neg_lo:[1,0,0] neg_hi:[1,0,0]
	v_pk_fma_f32 v[118:119], v[118:119], v[118:119], s[26:27] neg_lo:[1,0,0] neg_hi:[1,0,0]
	v_pk_fma_f32 v[120:121], v[120:121], v[120:121], s[20:21] neg_lo:[1,0,0] neg_hi:[1,0,0]
	v_pk_fma_f32 v[122:123], v[122:123], v[122:123], s[26:27] neg_lo:[1,0,0] neg_hi:[1,0,0]
	v_pk_fma_f32 v[124:125], v[124:125], v[124:125], s[24:25] neg_lo:[1,0,0] neg_hi:[1,0,0]
	v_pk_fma_f32 v[126:127], v[126:127], v[126:127], s[24:25] neg_lo:[1,0,0] neg_hi:[1,0,0]
	v_exp_f32_e32 v112, v112
	v_exp_f32_e32 v113, v113
	v_exp_f32_e32 v114, v114
	v_exp_f32_e32 v115, v115
	v_exp_f32_e32 v116, v116
	v_exp_f32_e32 v117, v117
	v_exp_f32_e32 v118, v118
	v_exp_f32_e32 v119, v119
	v_exp_f32_e32 v120, v120
	v_exp_f32_e32 v121, v121
	v_exp_f32_e32 v122, v122
	v_exp_f32_e32 v123, v123
	v_exp_f32_e32 v124, v124
	v_exp_f32_e32 v125, v125
	v_exp_f32_e32 v126, v126
	v_exp_f32_e32 v127, v127
	v_pk_add_f32 v[80:81], v[80:81], v[96:97]
	v_pk_fma_f32 v[84:85], v[96:97], v[48:49], v[84:85]
	v_pk_add_f32 v[82:83], v[82:83], v[102:103]
	v_pk_add_f32 v[80:81], v[80:81], v[98:99]
	v_pk_fma_f32 v[84:85], v[98:99], v[50:51], v[84:85]
	v_pk_fma_f32 v[86:87], v[102:103], v[50:51], v[86:87]
	v_pk_add_f32 v[80:81], v[80:81], v[100:101]
	v_pk_fma_f32 v[84:85], v[100:101], v[52:53], v[84:85]
	v_pk_add_f32 v[82:83], v[82:83], v[104:105]
	v_pk_fma_f32 v[86:87], v[104:105], v[52:53], v[86:87]
	v_pk_add_f32 v[80:81], v[80:81], v[108:109]
	v_pk_add_f32 v[82:83], v[82:83], v[106:107]
	v_pk_fma_f32 v[86:87], v[106:107], v[54:55], v[86:87]
	v_pk_fma_f32 v[84:85], v[108:109], v[50:51], v[84:85] op_sel:[0,1,0] op_sel_hi:[1,0,1]
	v_pk_add_f32 v[82:83], v[82:83], v[110:111]
	v_pk_fma_f32 v[86:87], v[110:111], v[52:53], v[86:87] op_sel:[0,1,0] op_sel_hi:[1,0,1]
	v_sub_f32_e32 v96, v49, v34
	v_sub_f32_e32 v98, v52, v35
	v_sub_f32_e32 v100, v51, v36
	v_sub_f32_e32 v102, v54, v37
	v_sub_f32_e32 v104, v49, v42
	v_sub_f32_e32 v106, v52, v43
	v_sub_f32_e32 v108, v51, v44
	v_sub_f32_e32 v110, v54, v45
	v_fma_f32 v96, -v96, v96, s26
	v_fma_f32 v98, -v98, v98, s26
	v_fma_f32 v100, -v100, v100, s26
	v_fma_f32 v102, -v102, v102, s26
	v_fma_f32 v104, -v104, v104, s24
	v_fma_f32 v106, -v106, v106, s24
	v_fma_f32 v108, -v108, v108, s24
	v_fma_f32 v110, -v110, v110, s24
	v_exp_f32_e32 v96, v96
	v_exp_f32_e32 v98, v98
	v_exp_f32_e32 v100, v100
	v_exp_f32_e32 v102, v102
	v_exp_f32_e32 v104, v104
	v_exp_f32_e32 v106, v106
	v_exp_f32_e32 v108, v108
	v_exp_f32_e32 v110, v110
	v_pk_add_f32 v[88:89], v[88:89], v[112:113]
	v_pk_fma_f32 v[92:93], v[112:113], v[48:49], v[92:93]
	v_pk_add_f32 v[90:91], v[90:91], v[118:119]
	v_pk_add_f32 v[88:89], v[88:89], v[114:115]
	v_pk_fma_f32 v[92:93], v[114:115], v[50:51], v[92:93]
	v_pk_fma_f32 v[94:95], v[118:119], v[50:51], v[94:95]
	v_pk_add_f32 v[88:89], v[88:89], v[116:117]
	v_pk_fma_f32 v[92:93], v[116:117], v[52:53], v[92:93]
	v_pk_add_f32 v[90:91], v[90:91], v[120:121]
	v_pk_fma_f32 v[94:95], v[120:121], v[52:53], v[94:95]
	v_pk_add_f32 v[88:89], v[88:89], v[124:125]
	v_pk_add_f32 v[90:91], v[90:91], v[122:123]
	v_pk_fma_f32 v[94:95], v[122:123], v[54:55], v[94:95]
	v_pk_fma_f32 v[92:93], v[124:125], v[50:51], v[92:93] op_sel:[0,1,0] op_sel_hi:[1,0,1]
	v_pk_add_f32 v[90:91], v[90:91], v[126:127]
	v_pk_fma_f32 v[94:95], v[126:127], v[52:53], v[94:95] op_sel:[0,1,0] op_sel_hi:[1,0,1]
	v_add_f32_e32 v80, v80, v96
	v_fmac_f32_e32 v84, v96, v49
	v_add_f32_e32 v81, v81, v98
	v_fmac_f32_e32 v85, v98, v52
	v_add_f32_e32 v82, v82, v100
	v_fmac_f32_e32 v86, v100, v51
	v_add_f32_e32 v83, v83, v102
	v_fmac_f32_e32 v87, v102, v54
	v_add_f32_e32 v88, v88, v104
	v_fmac_f32_e32 v92, v104, v49
	v_add_f32_e32 v89, v89, v106
	v_fmac_f32_e32 v93, v106, v52
	v_add_f32_e32 v90, v90, v108
	v_fmac_f32_e32 v94, v108, v51
	v_add_f32_e32 v91, v91, v110
	v_fmac_f32_e32 v95, v110, v54
	v_rcp_f32_e32 v96, v80
	v_rcp_f32_e32 v97, v81
	v_rcp_f32_e32 v98, v82
	v_rcp_f32_e32 v99, v83
	v_pk_mul_f32 v[84:85], v[84:85], s[34:35]
	v_pk_mul_f32 v[86:87], v[86:87], s[34:35]
	v_pk_mul_f32 v[84:85], v[84:85], v[96:97]
	v_pk_mul_f32 v[86:87], v[86:87], v[98:99]
	buffer_store_dwordx4 v[84:87], v135, s[12:15], 0 offen sc1
	s_waitcnt vmcnt(3)
	s_nop 0
	v_mov_b32_dpp v56, v60 row_shr:1 row_mask:0xf bank_mask:0xf
	v_mov_b32_dpp v57, v61 row_shr:1 row_mask:0xf bank_mask:0xf
	v_mov_b32_dpp v62, v58 row_shl:1 row_mask:0xf bank_mask:0xf
	v_mov_b32_dpp v63, v59 row_shl:1 row_mask:0xf bank_mask:0xf
	v_pk_mul_f32 v[58:59], v[58:59], s[32:33]
	v_pk_mul_f32 v[60:61], v[60:61], s[32:33]
	v_cndmask_b32_e64 v57, v57, v56, vcc
	v_cndmask_b32_e64 v62, v62, v63, s[16:17]
	v_pk_mul_f32 v[56:57], v[56:57], s[32:33]
	v_pk_mul_f32 v[62:63], v[62:63], s[32:33]
	v_pk_add_f32 v[96:97], v[56:57], v[42:43] neg_lo:[0,1] neg_hi:[0,1]
	v_pk_add_f32 v[98:99], v[58:59], v[42:43] neg_lo:[0,1] neg_hi:[0,1]
	v_pk_add_f32 v[100:101], v[60:61], v[42:43] neg_lo:[0,1] neg_hi:[0,1]
	v_pk_add_f32 v[102:103], v[58:59], v[44:45] neg_lo:[0,1] neg_hi:[0,1]
	v_pk_add_f32 v[104:105], v[60:61], v[44:45] neg_lo:[0,1] neg_hi:[0,1]
	v_pk_add_f32 v[106:107], v[62:63], v[44:45] neg_lo:[0,1] neg_hi:[0,1]
	v_pk_add_f32 v[108:109], v[58:59], v[42:43] op_sel:[1,0] op_sel_hi:[0,1] neg_lo:[0,1] neg_hi:[0,1]
	v_pk_add_f32 v[110:111], v[60:61], v[44:45] op_sel:[1,0] op_sel_hi:[0,1] neg_lo:[0,1] neg_hi:[0,1]
	v_pk_fma_f32 v[96:97], v[96:97], v[96:97], s[28:29] neg_lo:[1,0,0] neg_hi:[1,0,0]
	v_pk_fma_f32 v[98:99], v[98:99], v[98:99], s[22:23] neg_lo:[1,0,0] neg_hi:[1,0,0]
	v_pk_fma_f32 v[100:101], v[100:101], v[100:101], s[28:29] neg_lo:[1,0,0] neg_hi:[1,0,0]
	v_pk_fma_f32 v[102:103], v[102:103], v[102:103], s[28:29] neg_lo:[1,0,0] neg_hi:[1,0,0]
	v_pk_fma_f32 v[104:105], v[104:105], v[104:105], s[22:23] neg_lo:[1,0,0] neg_hi:[1,0,0]
	v_pk_fma_f32 v[106:107], v[106:107], v[106:107], s[28:29] neg_lo:[1,0,0] neg_hi:[1,0,0]
	v_pk_fma_f32 v[108:109], v[108:109], v[108:109], s[26:27] neg_lo:[1,0,0] neg_hi:[1,0,0]
	v_pk_fma_f32 v[110:111], v[110:111], v[110:111], s[26:27] neg_lo:[1,0,0] neg_hi:[1,0,0]
	v_exp_f32_e32 v96, v96
	v_exp_f32_e32 v97, v97
	v_exp_f32_e32 v98, v98
	v_exp_f32_e32 v99, v99
	v_exp_f32_e32 v100, v100
	v_exp_f32_e32 v101, v101
	v_exp_f32_e32 v102, v102
	v_exp_f32_e32 v103, v103
	v_exp_f32_e32 v104, v104
	v_exp_f32_e32 v105, v105
	v_exp_f32_e32 v106, v106
	v_exp_f32_e32 v107, v107
	v_exp_f32_e32 v108, v108
	v_exp_f32_e32 v109, v109
	v_exp_f32_e32 v110, v110
	v_exp_f32_e32 v111, v111
	v_sub_f32_e32 v112, v57, v42
	v_sub_f32_e32 v114, v60, v43
	v_sub_f32_e32 v116, v59, v44
	v_sub_f32_e32 v118, v62, v45
	v_fma_f32 v112, -v112, v112, s26
	v_fma_f32 v114, -v114, v114, s26
	v_fma_f32 v116, -v116, v116, s26
	v_fma_f32 v118, -v118, v118, s26
	v_exp_f32_e32 v112, v112
	v_exp_f32_e32 v114, v114
	v_exp_f32_e32 v116, v116
	v_exp_f32_e32 v118, v118
	v_pk_add_f32 v[88:89], v[88:89], v[96:97]
	v_pk_fma_f32 v[92:93], v[96:97], v[56:57], v[92:93]
	v_pk_add_f32 v[90:91], v[90:91], v[102:103]
	v_pk_add_f32 v[88:89], v[88:89], v[98:99]
	v_pk_fma_f32 v[92:93], v[98:99], v[58:59], v[92:93]
	v_pk_fma_f32 v[94:95], v[102:103], v[58:59], v[94:95]
	v_pk_add_f32 v[88:89], v[88:89], v[100:101]
	v_pk_fma_f32 v[92:93], v[100:101], v[60:61], v[92:93]
	v_pk_add_f32 v[90:91], v[90:91], v[104:105]
	v_pk_fma_f32 v[94:95], v[104:105], v[60:61], v[94:95]
	v_pk_add_f32 v[88:89], v[88:89], v[108:109]
	v_pk_add_f32 v[90:91], v[90:91], v[106:107]
	v_pk_fma_f32 v[94:95], v[106:107], v[62:63], v[94:95]
	v_pk_fma_f32 v[92:93], v[108:109], v[58:59], v[92:93] op_sel:[0,1,0] op_sel_hi:[1,0,1]
	v_pk_add_f32 v[90:91], v[90:91], v[110:111]
	v_pk_fma_f32 v[94:95], v[110:111], v[60:61], v[94:95] op_sel:[0,1,0] op_sel_hi:[1,0,1]
	v_add_f32_e32 v88, v88, v112
	v_fmac_f32_e32 v92, v112, v57
	v_add_f32_e32 v89, v89, v114
	v_fmac_f32_e32 v93, v114, v60
	v_add_f32_e32 v90, v90, v116
	v_fmac_f32_e32 v94, v116, v59
	v_add_f32_e32 v91, v91, v118
	v_fmac_f32_e32 v95, v118, v62
	v_rcp_f32_e32 v96, v88
	v_rcp_f32_e32 v97, v89
	v_rcp_f32_e32 v98, v90
	v_rcp_f32_e32 v99, v91
	v_pk_mul_f32 v[92:93], v[92:93], s[34:35]
	v_pk_mul_f32 v[94:95], v[94:95], s[34:35]
	v_pk_mul_f32 v[92:93], v[92:93], v[96:97]
	v_pk_mul_f32 v[94:95], v[94:95], v[98:99]
	buffer_store_dwordx4 v[92:95], v135, s[12:15], 0 offen offset:2048 sc1
	s_endpgm

	.amdhsa_kernel _Z16bilateral_kernelPKfS0_Pf
		.amdhsa_group_segment_fixed_size 0
		.amdhsa_private_segment_fixed_size 0
		.amdhsa_kernarg_size 24
		.amdhsa_user_sgpr_count 2
		.amdhsa_user_sgpr_dispatch_ptr 0
		.amdhsa_user_sgpr_queue_ptr 0
		.amdhsa_user_sgpr_kernarg_segment_ptr 1
		.amdhsa_user_sgpr_dispatch_id 0
		.amdhsa_user_sgpr_kernarg_preload_length 0
		.amdhsa_user_sgpr_kernarg_preload_offset 0
		.amdhsa_user_sgpr_private_segment_size 0
		.amdhsa_uses_dynamic_stack 0
		.amdhsa_enable_private_segment 0
		.amdhsa_system_sgpr_workgroup_id_x 1
		.amdhsa_system_sgpr_workgroup_id_y 0
		.amdhsa_system_sgpr_workgroup_id_z 0
		.amdhsa_system_sgpr_workgroup_info 0
		.amdhsa_system_vgpr_workitem_id 0
		.amdhsa_next_free_vgpr 160
		.amdhsa_next_free_sgpr 40
		.amdhsa_accum_offset 160
		.amdhsa_reserve_vcc 1
		.amdhsa_float_round_mode_32 0
		.amdhsa_float_round_mode_16_64 0
		.amdhsa_float_denorm_mode_32 3
		.amdhsa_float_denorm_mode_16_64 3
		.amdhsa_dx10_clamp 1
		.amdhsa_ieee_mode 1
		.amdhsa_fp16_overflow 0
		.amdhsa_tg_split 0
		.amdhsa_exception_fp_ieee_invalid_op 0
		.amdhsa_exception_fp_denorm_src 0
		.amdhsa_exception_fp_ieee_div_zero 0
		.amdhsa_exception_fp_ieee_overflow 0
		.amdhsa_exception_fp_ieee_underflow 0
		.amdhsa_exception_fp_ieee_inexact 0
		.amdhsa_exception_int_div_zero 0
	.end_amdhsa_kernel

amdhsa.kernels:
  - .agpr_count:     0
    .args:
      - .actual_access:  read_only
        .address_space:  global
        .offset:         0
        .size:           8
        .value_kind:     global_buffer
      - .actual_access:  read_only
        .address_space:  global
        .offset:         8
        .size:           8
        .value_kind:     global_buffer
      - .actual_access:  write_only
        .address_space:  global
        .offset:         16
        .size:           8
        .value_kind:     global_buffer
    .group_segment_fixed_size: 0
    .kernarg_segment_align: 8
    .kernarg_segment_size: 24
    .language:       OpenCL C
    .language_version:
      - 2
      - 0
    .max_flat_workgroup_size: 256
    .name:           _Z16bilateral_kernelPKfS0_Pf
    .private_segment_fixed_size: 0
    .sgpr_count:     46
    .sgpr_spill_count: 0
    .symbol:         _Z16bilateral_kernelPKfS0_Pf.kd
    .uniform_work_group_size: 1
    .uses_dynamic_stack: false
    .vgpr_count:     160
    .vgpr_spill_count: 0
    .wavefront_size: 64
